# v17 + MF=8 loops: tail staging block interleaved into MFMA group 14 (no exposed ds_write before barrier)
# speedup vs baseline: 1.0371x; 1.0037x over previous
; #define G_ENDTILE(VM) do { asm volatile("s_waitcnt vmcnt(" #VM ")" ::: "memory"); \
;         asm volatile("s_waitcnt lgkmcnt(0)" ::: "memory"); __builtin_amdgcn_s_barrier(); asm volatile("" ::: "memory"); } while (0)
;     ...
;         for (int t = 0; t < nt - 2; t += 2) {
;             G_TILE(G_A0, G_B0, true, G_B1, G_A1, t + 1, true, t + 2, (void)0);
;             G_ENDTILE(8);
.LBB0_71:
	s_mov_b32 m0, s68
	s_add_i32 s25, s24, 0xffffff80
	ds_read_b64_tr_b16 v[170:171], v166
	ds_read_b64_tr_b16 v[172:173], v167
	ds_read_b64_tr_b16 v[176:177], v167 offset:32
	ds_read_b128 v[178:181], v162
	ds_read_b64_tr_b16 v[174:175], v166 offset:32
	ds_read_b64_tr_b16 v[182:183], v166 offset:64
	ds_read_b64_tr_b16 v[186:187], v166 offset:96
	ds_read_b64_tr_b16 v[184:185], v167 offset:64
	ds_read_b64_tr_b16 v[188:189], v167 offset:96
	ds_read_b128 v[190:193], v162 offset:2048
	ds_read_b128 v[194:197], v162 offset:4096
	buffer_load_dwordx4 v163, s[20:23], s25 offen lds
	s_mov_b32 m0, s67
	v_mfma_f32_16x16x32_bf16 v[44:47], v[244:247], v[252:255], v[44:47]
	v_mfma_f32_16x16x32_bf16 v[40:43], v[248:251], v[252:255], v[40:43]
	v_mfma_f32_16x16x32_bf16 v[36:39], v[198:201], v[252:255], v[36:39]
	v_mfma_f32_16x16x32_bf16 v[32:35], v[202:205], v[252:255], v[32:35]
	s_waitcnt lgkmcnt(7)
	v_mfma_f32_16x16x32_bf16 v[156:159], v[170:173], v[178:181], v[156:159]
	buffer_load_dwordx4 v165, s[20:23], s25 offen lds
	s_waitcnt lgkmcnt(6)
	v_mfma_f32_16x16x32_bf16 v[152:155], v[174:177], v[178:181], v[152:155]
	s_waitcnt lgkmcnt(3)
	v_mfma_f32_16x16x32_bf16 v[148:151], v[182:185], v[178:181], v[148:151]
	s_waitcnt lgkmcnt(2)
	v_mfma_f32_16x16x32_bf16 v[144:147], v[186:189], v[178:181], v[144:147]
	s_waitcnt lgkmcnt(1)
	v_mfma_f32_16x16x32_bf16 v[140:143], v[170:173], v[190:193], v[140:143]
	s_mov_b32 m0, s66
	s_nop 0
	buffer_load_dwordx4 v164, s[20:23], s25 offen lds
	ds_read_b128 v[178:181], v162 offset:6144
	s_waitcnt vmcnt(10)
	v_cvt_pk_bf16_f32 v15, v14, v15
	v_cvt_pk_bf16_f32 v14, v12, v13
	v_mfma_f32_16x16x32_bf16 v[136:139], v[174:177], v[190:193], v[136:139]
	ds_write_b64 v161, v[14:15] offset:34816
	v_mfma_f32_16x16x32_bf16 v[132:135], v[182:185], v[190:193], v[132:135]
	s_mov_b32 m0, s65
	s_nop 0
	buffer_load_dwordx4 v168, s[20:23], s25 offen lds
	s_add_i32 s25, s9, 0xffd60000
	v_mfma_f32_16x16x32_bf16 v[128:131], v[186:189], v[190:193], v[128:131]
	s_waitcnt lgkmcnt(2)
	v_mfma_f32_16x16x32_bf16 v[124:127], v[170:173], v[194:197], v[124:127]
	ds_read_b128 v[190:193], v162 offset:8192
	v_mfma_f32_16x16x32_bf16 v[120:123], v[174:177], v[194:197], v[120:123]
	v_mfma_f32_16x16x32_bf16 v[116:119], v[182:185], v[194:197], v[116:119]
	v_mfma_f32_16x16x32_bf16 v[112:115], v[186:189], v[194:197], v[112:115]
	s_waitcnt lgkmcnt(2)
	v_mfma_f32_16x16x32_bf16 v[108:111], v[170:173], v[178:181], v[108:111]
	ds_read_b128 v[194:197], v162 offset:10240
	buffer_load_dwordx4 v[12:15], v160, s[12:15], s25 offen
	s_waitcnt vmcnt(11)
	v_cvt_pk_bf16_f32 v3, v2, v3
	v_cvt_pk_bf16_f32 v2, v0, v1
	v_mfma_f32_16x16x32_bf16 v[104:107], v[174:177], v[178:181], v[104:107]
	ds_write_b64 v161, v[2:3] offset:43520
	v_mfma_f32_16x16x32_bf16 v[100:103], v[182:185], v[178:181], v[100:103]
	v_mfma_f32_16x16x32_bf16 v[96:99], v[186:189], v[178:181], v[96:99]
	s_add_i32 s26, s9, 0xffdc0000
	s_waitcnt lgkmcnt(2)
	v_mfma_f32_16x16x32_bf16 v[92:95], v[170:173], v[190:193], v[92:95]
	ds_read_b128 v[178:181], v162 offset:12288
	v_mfma_f32_16x16x32_bf16 v[88:91], v[174:177], v[190:193], v[88:91]
	v_mfma_f32_16x16x32_bf16 v[84:87], v[182:185], v[190:193], v[84:87]
	v_mfma_f32_16x16x32_bf16 v[80:83], v[186:189], v[190:193], v[80:83]
	s_waitcnt lgkmcnt(2)
	v_mfma_f32_16x16x32_bf16 v[76:79], v[170:173], v[194:197], v[76:79]
	ds_read_b128 v[190:193], v162 offset:14336
	buffer_load_dwordx4 v[0:3], v160, s[12:15], s26 offen
	s_waitcnt vmcnt(11)
	v_cvt_pk_bf16_f32 v31, v30, v31
	v_cvt_pk_bf16_f32 v30, v28, v29
	v_mfma_f32_16x16x32_bf16 v[72:75], v[174:177], v[194:197], v[72:75]
	ds_write_b64 v161, v[30:31] offset:52224
	v_mfma_f32_16x16x32_bf16 v[68:71], v[182:185], v[194:197], v[68:71]
	v_mfma_f32_16x16x32_bf16 v[64:67], v[186:189], v[194:197], v[64:67]
	s_add_i32 s27, s9, 0xffe20000
	s_waitcnt lgkmcnt(2)
	v_mfma_f32_16x16x32_bf16 v[60:63], v[170:173], v[178:181], v[60:63]
	ds_read_b128 v[194:197], v162 offset:1024
	v_mfma_f32_16x16x32_bf16 v[56:59], v[174:177], v[178:181], v[56:59]
	v_mfma_f32_16x16x32_bf16 v[52:55], v[182:185], v[178:181], v[52:55]
	v_mfma_f32_16x16x32_bf16 v[48:51], v[186:189], v[178:181], v[48:51]
	s_waitcnt lgkmcnt(2)
	v_mfma_f32_16x16x32_bf16 v[44:47], v[170:173], v[190:193], v[44:47]
	ds_read_b128 v[170:173], v162 offset:3072
	buffer_load_dwordx4 v[28:31], v160, s[12:15], s27 offen
	s_waitcnt vmcnt(11)
	v_cvt_pk_bf16_f32 v27, v26, v27
	v_cvt_pk_bf16_f32 v26, v24, v25
	v_mfma_f32_16x16x32_bf16 v[40:43], v[174:177], v[190:193], v[40:43]
	ds_read_b64_tr_b16 v[244:245], v166 offset:17408
	ds_read_b64_tr_b16 v[248:249], v166 offset:17440
	ds_read_b64_tr_b16 v[198:199], v166 offset:17472
	ds_read_b64_tr_b16 v[202:203], v166 offset:17504
	ds_read_b64_tr_b16 v[246:247], v167 offset:17408
	ds_read_b64_tr_b16 v[250:251], v167 offset:17440
	ds_read_b64_tr_b16 v[200:201], v167 offset:17472
	ds_read_b64_tr_b16 v[204:205], v167 offset:17504
	ds_write_b64 v161, v[26:27] offset:60928
	v_mfma_f32_16x16x32_bf16 v[36:39], v[182:185], v[190:193], v[36:39]
	v_mfma_f32_16x16x32_bf16 v[32:35], v[186:189], v[190:193], v[32:35]
	s_add_i32 s42, s9, 0xffe80000
	s_waitcnt lgkmcnt(4)
	v_mfma_f32_16x16x32_bf16 v[156:159], v[244:247], v[194:197], v[156:159]
	ds_read_b128 v[182:185], v162 offset:5120
	s_waitcnt lgkmcnt(4)
	v_mfma_f32_16x16x32_bf16 v[152:155], v[248:251], v[194:197], v[152:155]
	s_waitcnt lgkmcnt(3)
	v_mfma_f32_16x16x32_bf16 v[148:151], v[198:201], v[194:197], v[148:151]
	s_waitcnt lgkmcnt(2)
	v_mfma_f32_16x16x32_bf16 v[144:147], v[202:205], v[194:197], v[144:147]
	v_mfma_f32_16x16x32_bf16 v[140:143], v[244:247], v[170:173], v[140:143]
	ds_read_b128 v[186:189], v162 offset:7168
	buffer_load_dwordx4 v[24:27], v160, s[12:15], s42 offen
	s_waitcnt vmcnt(11)
; #define G_DMA_A(kt, AO) do { G_DMA1(kt, AO, 0); G_DMA1(kt, AO, 1); G_DMA1(kt, AO, 2); G_DMA1(kt, AO, 3); if (MF == 9) G_DMA5(kt, AO); } while (0)
; #define G_ISSUE_B(kt) do { const unsigned _sb = (unsigned)(kt) * 4u * kstepB; \
;         _Pragma("unroll") for (int _i = 0; _i < 8; ++_i) sb[_i] = bload16(_i < 4 ? rsB0 : rsB1, vob, _sb + (_i & 3) * kstepB); } while (0)
; #define G_WRITE_B(BO) do { \
;         _Pragma("unroll") for (int _i = 0; _i < 8; ++_i) *(LAS u32x2*)(b_wr + (BO) + (_i & 3) * (16 * G_BSTRIDE) + (_i >> 2) * SLAB1) = pack4(__builtin_bit_cast(f32x4, sb[_i])); } while (0)
; #define G_ENDTILE(VM) do { asm volatile("s_waitcnt vmcnt(" #VM ")" ::: "memory"); \
;         asm volatile("s_waitcnt lgkmcnt(0)" ::: "memory"); __builtin_amdgcn_s_barrier(); asm volatile("" ::: "memory"); } while (0)
;     ...
;     __builtin_amdgcn_s_barrier();
;     G_DMA_A(0, G_A0); G_ISSUE_B(0); G_WRITE_B(G_B0);
;     __builtin_amdgcn_sched_barrier(0);
;     G_ISSUE_B(1);
;     __builtin_amdgcn_sched_barrier(0);
;     G_ENDTILE(8);
;     for (int ui = 0;; ++ui) {
; #pragma unroll
;         for (int m = 0; m < MF; ++m)
; #pragma unroll
;             for (int n = 0; n < 4; ++n) acc[m][n] = (f32x4){0.f, 0.f, 0.f, 0.f};
;         for (int t = 0; t < nt - 2; t += 2) {
;             G_TILE(G_A0, G_B0, true, G_B1, G_A1, t + 1, true, t + 2, (void)0);
;             G_ENDTILE(8);
;             G_TILE(G_A1, G_B1, true, G_B0, G_A0, t + 2, true, t + 3, (void)0);
;             G_ENDTILE(8);
	v_cvt_pk_bf16_f32 v23, v22, v23
	v_cvt_pk_bf16_f32 v22, v20, v21
	v_mfma_f32_16x16x32_bf16 v[136:139], v[248:251], v[170:173], v[136:139]
	ds_write_b64 v161, v[22:23] offset:35072
	v_mfma_f32_16x16x32_bf16 v[132:135], v[198:201], v[170:173], v[132:135]
	v_mfma_f32_16x16x32_bf16 v[128:131], v[202:205], v[170:173], v[128:131]
	s_waitcnt lgkmcnt(2)
	v_mfma_f32_16x16x32_bf16 v[124:127], v[244:247], v[182:185], v[124:127]
	ds_read_b128 v[170:173], v162 offset:9216
	v_mfma_f32_16x16x32_bf16 v[120:123], v[248:251], v[182:185], v[120:123]
	v_mfma_f32_16x16x32_bf16 v[116:119], v[198:201], v[182:185], v[116:119]
	v_mfma_f32_16x16x32_bf16 v[112:115], v[202:205], v[182:185], v[112:115]
	s_waitcnt lgkmcnt(2)
	v_mfma_f32_16x16x32_bf16 v[108:111], v[244:247], v[186:189], v[108:111]
	ds_read_b128 v[182:185], v162 offset:11264
	buffer_load_dwordx4 v[20:23], v160, s[16:19], s25 offen
	s_waitcnt vmcnt(11)
	v_cvt_pk_bf16_f32 v7, v6, v7
	v_cvt_pk_bf16_f32 v6, v4, v5
	v_mfma_f32_16x16x32_bf16 v[104:107], v[248:251], v[186:189], v[104:107]
	ds_write_b64 v161, v[6:7] offset:43776
	v_mfma_f32_16x16x32_bf16 v[100:103], v[198:201], v[186:189], v[100:103]
	v_mfma_f32_16x16x32_bf16 v[96:99], v[202:205], v[186:189], v[96:99]
	s_waitcnt lgkmcnt(2)
	v_mfma_f32_16x16x32_bf16 v[92:95], v[244:247], v[170:173], v[92:95]
	ds_read_b128 v[186:189], v162 offset:13312
	v_mfma_f32_16x16x32_bf16 v[88:91], v[248:251], v[170:173], v[88:91]
	v_mfma_f32_16x16x32_bf16 v[84:87], v[198:201], v[170:173], v[84:87]
	v_mfma_f32_16x16x32_bf16 v[80:83], v[202:205], v[170:173], v[80:83]
	s_waitcnt lgkmcnt(2)
	v_mfma_f32_16x16x32_bf16 v[76:79], v[244:247], v[182:185], v[76:79]
	ds_read_b128 v[252:255], v162 offset:15360
	buffer_load_dwordx4 v[4:7], v160, s[16:19], s26 offen
	s_waitcnt vmcnt(11)
	v_cvt_pk_bf16_f32 v11, v10, v11
	v_cvt_pk_bf16_f32 v10, v8, v9
	v_mfma_f32_16x16x32_bf16 v[72:75], v[248:251], v[182:185], v[72:75]
	ds_write_b64 v161, v[10:11] offset:52480
	v_mfma_f32_16x16x32_bf16 v[68:71], v[198:201], v[182:185], v[68:71]
	v_mfma_f32_16x16x32_bf16 v[64:67], v[202:205], v[182:185], v[64:67]
	s_waitcnt lgkmcnt(2)
	v_mfma_f32_16x16x32_bf16 v[60:63], v[244:247], v[186:189], v[60:63]
	buffer_load_dwordx4 v[8:11], v160, s[16:19], s27 offen
	s_waitcnt vmcnt(11)
	v_cvt_pk_bf16_f32 v19, v18, v19
	v_cvt_pk_bf16_f32 v18, v16, v17
	v_mfma_f32_16x16x32_bf16 v[56:59], v[248:251], v[186:189], v[56:59]
	ds_write_b64 v161, v[18:19] offset:61184
	v_mfma_f32_16x16x32_bf16 v[52:55], v[198:201], v[186:189], v[52:55]
	buffer_load_dwordx4 v[16:19], v160, s[16:19], s42 offen
	v_mfma_f32_16x16x32_bf16 v[48:51], v[202:205], v[186:189], v[48:51]
	s_waitcnt vmcnt(8)
	s_mov_b32 m0, s55
	s_waitcnt lgkmcnt(0)
	s_barrier
	ds_read_b64_tr_b16 v[170:171], v166 offset:34816
	ds_read_b64_tr_b16 v[172:173], v167 offset:34816
	ds_read_b64_tr_b16 v[176:177], v167 offset:34848
	ds_read_b128 v[178:181], v162 offset:32768
	ds_read_b64_tr_b16 v[174:175], v166 offset:34848
	ds_read_b64_tr_b16 v[182:183], v166 offset:34880
	ds_read_b64_tr_b16 v[186:187], v166 offset:34912
	ds_read_b64_tr_b16 v[184:185], v167 offset:34880
	ds_read_b64_tr_b16 v[188:189], v167 offset:34912
	ds_read_b128 v[190:193], v162 offset:34816
	ds_read_b128 v[194:197], v162 offset:36864
	buffer_load_dwordx4 v163, s[20:23], s24 offen lds
	s_mov_b32 m0, s56
	v_mfma_f32_16x16x32_bf16 v[44:47], v[244:247], v[252:255], v[44:47]
	v_mfma_f32_16x16x32_bf16 v[40:43], v[248:251], v[252:255], v[40:43]
	v_mfma_f32_16x16x32_bf16 v[36:39], v[198:201], v[252:255], v[36:39]
	v_mfma_f32_16x16x32_bf16 v[32:35], v[202:205], v[252:255], v[32:35]
	s_waitcnt lgkmcnt(7)
	v_mfma_f32_16x16x32_bf16 v[156:159], v[170:173], v[178:181], v[156:159]
	buffer_load_dwordx4 v165, s[20:23], s24 offen lds
	s_add_i32 s25, s9, 0xffee0000
	s_waitcnt lgkmcnt(6)
	v_mfma_f32_16x16x32_bf16 v[152:155], v[174:177], v[178:181], v[152:155]
	s_waitcnt lgkmcnt(3)
	v_mfma_f32_16x16x32_bf16 v[148:151], v[182:185], v[178:181], v[148:151]
	s_waitcnt lgkmcnt(2)
	v_mfma_f32_16x16x32_bf16 v[144:147], v[186:189], v[178:181], v[144:147]
	s_waitcnt lgkmcnt(1)
	v_mfma_f32_16x16x32_bf16 v[140:143], v[170:173], v[190:193], v[140:143]
	s_mov_b32 m0, s57
	s_nop 0
	buffer_load_dwordx4 v164, s[20:23], s24 offen lds
	ds_read_b128 v[178:181], v162 offset:38912
	s_waitcnt vmcnt(10)
	v_cvt_pk_bf16_f32 v15, v14, v15
	v_cvt_pk_bf16_f32 v14, v12, v13
	v_mfma_f32_16x16x32_bf16 v[136:139], v[174:177], v[190:193], v[136:139]
	ds_write_b64 v161, v[14:15]
	v_mfma_f32_16x16x32_bf16 v[132:135], v[182:185], v[190:193], v[132:135]
	s_mov_b32 m0, s59
	s_nop 0
	buffer_load_dwordx4 v168, s[20:23], s24 offen lds
	v_mfma_f32_16x16x32_bf16 v[128:131], v[186:189], v[190:193], v[128:131]
	s_waitcnt lgkmcnt(2)
	v_mfma_f32_16x16x32_bf16 v[124:127], v[170:173], v[194:197], v[124:127]
	ds_read_b128 v[190:193], v162 offset:40960
	v_mfma_f32_16x16x32_bf16 v[120:123], v[174:177], v[194:197], v[120:123]
	v_mfma_f32_16x16x32_bf16 v[116:119], v[182:185], v[194:197], v[116:119]
	v_mfma_f32_16x16x32_bf16 v[112:115], v[186:189], v[194:197], v[112:115]
	s_waitcnt lgkmcnt(2)
	v_mfma_f32_16x16x32_bf16 v[108:111], v[170:173], v[178:181], v[108:111]
	ds_read_b128 v[194:197], v162 offset:43008
	buffer_load_dwordx4 v[12:15], v160, s[12:15], s25 offen
	s_waitcnt vmcnt(11)
	v_cvt_pk_bf16_f32 v3, v2, v3
	v_cvt_pk_bf16_f32 v2, v0, v1
	v_mfma_f32_16x16x32_bf16 v[104:107], v[174:177], v[178:181], v[104:107]
	ds_write_b64 v161, v[2:3] offset:8704
	v_mfma_f32_16x16x32_bf16 v[100:103], v[182:185], v[178:181], v[100:103]
	v_mfma_f32_16x16x32_bf16 v[96:99], v[186:189], v[178:181], v[96:99]
	s_add_i32 s26, s9, 0xfff40000
	s_waitcnt lgkmcnt(2)
; #define G_DMA_A(kt, AO) do { G_DMA1(kt, AO, 0); G_DMA1(kt, AO, 1); G_DMA1(kt, AO, 2); G_DMA1(kt, AO, 3); if (MF == 9) G_DMA5(kt, AO); } while (0)
; #define G_ISSUE_B(kt) do { const unsigned _sb = (unsigned)(kt) * 4u * kstepB; \
;         _Pragma("unroll") for (int _i = 0; _i < 8; ++_i) sb[_i] = bload16(_i < 4 ? rsB0 : rsB1, vob, _sb + (_i & 3) * kstepB); } while (0)
; #define G_WRITE_B(BO) do { \
;         _Pragma("unroll") for (int _i = 0; _i < 8; ++_i) *(LAS u32x2*)(b_wr + (BO) + (_i & 3) * (16 * G_BSTRIDE) + (_i >> 2) * SLAB1) = pack4(__builtin_bit_cast(f32x4, sb[_i])); } while (0)
; #define G_ENDTILE(VM) do { asm volatile("s_waitcnt vmcnt(" #VM ")" ::: "memory"); \
;         asm volatile("s_waitcnt lgkmcnt(0)" ::: "memory"); __builtin_amdgcn_s_barrier(); asm volatile("" ::: "memory"); } while (0)
;     ...
;     __builtin_amdgcn_s_barrier();
;     G_DMA_A(0, G_A0); G_ISSUE_B(0); G_WRITE_B(G_B0);
;     __builtin_amdgcn_sched_barrier(0);
;     G_ISSUE_B(1);
;     __builtin_amdgcn_sched_barrier(0);
;     G_ENDTILE(8);
;     for (int ui = 0;; ++ui) {
; #pragma unroll
;         for (int m = 0; m < MF; ++m)
; #pragma unroll
;             for (int n = 0; n < 4; ++n) acc[m][n] = (f32x4){0.f, 0.f, 0.f, 0.f};
;         for (int t = 0; t < nt - 2; t += 2) {
;             G_TILE(G_A0, G_B0, true, G_B1, G_A1, t + 1, true, t + 2, (void)0);
;             G_ENDTILE(8);
;             G_TILE(G_A1, G_B1, true, G_B0, G_A0, t + 2, true, t + 3, (void)0);
;             G_ENDTILE(8);
;         }
	v_mfma_f32_16x16x32_bf16 v[92:95], v[170:173], v[190:193], v[92:95]
	ds_read_b128 v[178:181], v162 offset:45056
	v_mfma_f32_16x16x32_bf16 v[88:91], v[174:177], v[190:193], v[88:91]
	v_mfma_f32_16x16x32_bf16 v[84:87], v[182:185], v[190:193], v[84:87]
	v_mfma_f32_16x16x32_bf16 v[80:83], v[186:189], v[190:193], v[80:83]
	s_waitcnt lgkmcnt(2)
	v_mfma_f32_16x16x32_bf16 v[76:79], v[170:173], v[194:197], v[76:79]
	ds_read_b128 v[190:193], v162 offset:47104
	buffer_load_dwordx4 v[0:3], v160, s[12:15], s26 offen
	s_waitcnt vmcnt(11)
	v_cvt_pk_bf16_f32 v31, v30, v31
	v_cvt_pk_bf16_f32 v30, v28, v29
	v_mfma_f32_16x16x32_bf16 v[72:75], v[174:177], v[194:197], v[72:75]
	ds_write_b64 v161, v[30:31] offset:17408
	v_mfma_f32_16x16x32_bf16 v[68:71], v[182:185], v[194:197], v[68:71]
	v_mfma_f32_16x16x32_bf16 v[64:67], v[186:189], v[194:197], v[64:67]
	s_add_i32 s27, s9, 0xfffa0000
	s_waitcnt lgkmcnt(2)
	v_mfma_f32_16x16x32_bf16 v[60:63], v[170:173], v[178:181], v[60:63]
	ds_read_b128 v[194:197], v162 offset:33792
	v_mfma_f32_16x16x32_bf16 v[56:59], v[174:177], v[178:181], v[56:59]
	v_mfma_f32_16x16x32_bf16 v[52:55], v[182:185], v[178:181], v[52:55]
	v_mfma_f32_16x16x32_bf16 v[48:51], v[186:189], v[178:181], v[48:51]
	s_waitcnt lgkmcnt(2)
	v_mfma_f32_16x16x32_bf16 v[44:47], v[170:173], v[190:193], v[44:47]
	ds_read_b128 v[170:173], v162 offset:35840
	buffer_load_dwordx4 v[28:31], v160, s[12:15], s27 offen
	s_waitcnt vmcnt(11)
	v_cvt_pk_bf16_f32 v27, v26, v27
	v_cvt_pk_bf16_f32 v26, v24, v25
	v_mfma_f32_16x16x32_bf16 v[40:43], v[174:177], v[190:193], v[40:43]
	ds_read_b64_tr_b16 v[244:245], v166 offset:52224
	ds_read_b64_tr_b16 v[248:249], v166 offset:52256
	ds_read_b64_tr_b16 v[198:199], v166 offset:52288
	ds_read_b64_tr_b16 v[202:203], v166 offset:52320
	ds_read_b64_tr_b16 v[246:247], v167 offset:52224
	ds_read_b64_tr_b16 v[250:251], v167 offset:52256
	ds_read_b64_tr_b16 v[200:201], v167 offset:52288
	ds_read_b64_tr_b16 v[204:205], v167 offset:52320
	ds_write_b64 v161, v[26:27] offset:26112
	v_mfma_f32_16x16x32_bf16 v[36:39], v[182:185], v[190:193], v[36:39]
	v_mfma_f32_16x16x32_bf16 v[32:35], v[186:189], v[190:193], v[32:35]
	s_waitcnt lgkmcnt(4)
	v_mfma_f32_16x16x32_bf16 v[156:159], v[244:247], v[194:197], v[156:159]
	ds_read_b128 v[182:185], v162 offset:37888
	s_waitcnt lgkmcnt(4)
	v_mfma_f32_16x16x32_bf16 v[152:155], v[248:251], v[194:197], v[152:155]
	s_waitcnt lgkmcnt(3)
	v_mfma_f32_16x16x32_bf16 v[148:151], v[198:201], v[194:197], v[148:151]
	s_waitcnt lgkmcnt(2)
	v_mfma_f32_16x16x32_bf16 v[144:147], v[202:205], v[194:197], v[144:147]
	v_mfma_f32_16x16x32_bf16 v[140:143], v[244:247], v[170:173], v[140:143]
	ds_read_b128 v[186:189], v162 offset:39936
	buffer_load_dwordx4 v[24:27], v160, s[12:15], s9 offen
	s_waitcnt vmcnt(11)
	v_cvt_pk_bf16_f32 v23, v22, v23
	v_cvt_pk_bf16_f32 v22, v20, v21
	v_mfma_f32_16x16x32_bf16 v[136:139], v[248:251], v[170:173], v[136:139]
	ds_write_b64 v161, v[22:23] offset:256
	v_mfma_f32_16x16x32_bf16 v[132:135], v[198:201], v[170:173], v[132:135]
	v_mfma_f32_16x16x32_bf16 v[128:131], v[202:205], v[170:173], v[128:131]
	s_waitcnt lgkmcnt(2)
	v_mfma_f32_16x16x32_bf16 v[124:127], v[244:247], v[182:185], v[124:127]
	ds_read_b128 v[170:173], v162 offset:41984
	v_mfma_f32_16x16x32_bf16 v[120:123], v[248:251], v[182:185], v[120:123]
	v_mfma_f32_16x16x32_bf16 v[116:119], v[198:201], v[182:185], v[116:119]
	v_mfma_f32_16x16x32_bf16 v[112:115], v[202:205], v[182:185], v[112:115]
	s_waitcnt lgkmcnt(2)
	v_mfma_f32_16x16x32_bf16 v[108:111], v[244:247], v[186:189], v[108:111]
	ds_read_b128 v[182:185], v162 offset:44032
	buffer_load_dwordx4 v[20:23], v160, s[16:19], s25 offen
	s_waitcnt vmcnt(11)
	v_cvt_pk_bf16_f32 v7, v6, v7
	v_cvt_pk_bf16_f32 v6, v4, v5
	v_mfma_f32_16x16x32_bf16 v[104:107], v[248:251], v[186:189], v[104:107]
	ds_write_b64 v161, v[6:7] offset:8960
	v_mfma_f32_16x16x32_bf16 v[100:103], v[198:201], v[186:189], v[100:103]
	v_mfma_f32_16x16x32_bf16 v[96:99], v[202:205], v[186:189], v[96:99]
	s_waitcnt lgkmcnt(2)
	v_mfma_f32_16x16x32_bf16 v[92:95], v[244:247], v[170:173], v[92:95]
	ds_read_b128 v[186:189], v162 offset:46080
	v_mfma_f32_16x16x32_bf16 v[88:91], v[248:251], v[170:173], v[88:91]
	v_mfma_f32_16x16x32_bf16 v[84:87], v[198:201], v[170:173], v[84:87]
	v_mfma_f32_16x16x32_bf16 v[80:83], v[202:205], v[170:173], v[80:83]
	s_waitcnt lgkmcnt(2)
	v_mfma_f32_16x16x32_bf16 v[76:79], v[244:247], v[182:185], v[76:79]
	ds_read_b128 v[252:255], v162 offset:48128
	buffer_load_dwordx4 v[4:7], v160, s[16:19], s26 offen
	s_waitcnt vmcnt(11)
	v_cvt_pk_bf16_f32 v11, v10, v11
	v_cvt_pk_bf16_f32 v10, v8, v9
	v_mfma_f32_16x16x32_bf16 v[72:75], v[248:251], v[182:185], v[72:75]
	ds_write_b64 v161, v[10:11] offset:17664
	v_mfma_f32_16x16x32_bf16 v[68:71], v[198:201], v[182:185], v[68:71]
	v_mfma_f32_16x16x32_bf16 v[64:67], v[202:205], v[182:185], v[64:67]
	s_waitcnt lgkmcnt(2)
	v_mfma_f32_16x16x32_bf16 v[60:63], v[244:247], v[186:189], v[60:63]
	buffer_load_dwordx4 v[8:11], v160, s[16:19], s27 offen
	s_waitcnt vmcnt(11)
	v_cvt_pk_bf16_f32 v19, v18, v19
	v_cvt_pk_bf16_f32 v18, v16, v17
	v_mfma_f32_16x16x32_bf16 v[56:59], v[248:251], v[186:189], v[56:59]
	ds_write_b64 v161, v[18:19] offset:26368
	v_mfma_f32_16x16x32_bf16 v[52:55], v[198:201], v[186:189], v[52:55]
	buffer_load_dwordx4 v[16:19], v160, s[16:19], s9 offen
	v_mfma_f32_16x16x32_bf16 v[48:51], v[202:205], v[186:189], v[48:51]
	s_waitcnt vmcnt(8)
	s_waitcnt lgkmcnt(0)
	s_barrier
	s_add_i32 s8, s8, 2
	s_add_i32 s9, s9, 0x300000
	s_addk_i32 s24, 0x100
	s_cmp_ge_i32 s8, s64
	s_cbranch_scc0 .LBB0_71
	v_mfma_f32_16x16x32_bf16 v[44:47], v[244:247], v[252:255], v[44:47]
	v_mfma_f32_16x16x32_bf16 v[40:43], v[248:251], v[252:255], v[40:43]
	v_mfma_f32_16x16x32_bf16 v[36:39], v[198:201], v[252:255], v[36:39]
	v_mfma_f32_16x16x32_bf16 v[32:35], v[202:205], v[252:255], v[32:35]
	s_branch .LBB0_73

; #define G_DMA_A(kt, AO) do { G_DMA1(kt, AO, 0); G_DMA1(kt, AO, 1); G_DMA1(kt, AO, 2); G_DMA1(kt, AO, 3); if (MF == 9) G_DMA5(kt, AO); } while (0)
; #define G_ISSUE_B(kt) do { const unsigned _sb = (unsigned)(kt) * 4u * kstepB; \
;         _Pragma("unroll") for (int _i = 0; _i < 8; ++_i) sb[_i] = bload16(_i < 4 ? rsB0 : rsB1, vob, _sb + (_i & 3) * kstepB); } while (0)
; #define G_WRITE_B(BO) do { \
;         _Pragma("unroll") for (int _i = 0; _i < 8; ++_i) *(LAS u32x2*)(b_wr + (BO) + (_i & 3) * (16 * G_BSTRIDE) + (_i >> 2) * SLAB1) = pack4(__builtin_bit_cast(f32x4, sb[_i])); } while (0)
; #define G_ENDTILE(VM) do { asm volatile("s_waitcnt vmcnt(" #VM ")" ::: "memory"); \
;         asm volatile("s_waitcnt lgkmcnt(0)" ::: "memory"); __builtin_amdgcn_s_barrier(); asm volatile("" ::: "memory"); } while (0)
;     ...
;     __builtin_amdgcn_s_barrier();
;     G_DMA_A(0, G_A0); G_ISSUE_B(0); G_WRITE_B(G_B0);
;     __builtin_amdgcn_sched_barrier(0);
;     G_ISSUE_B(1);
;     __builtin_amdgcn_sched_barrier(0);
;     G_ENDTILE(8);
;     for (int ui = 0;; ++ui) {
; #pragma unroll
;         for (int m = 0; m < MF; ++m)
; #pragma unroll
;             for (int n = 0; n < 4; ++n) acc[m][n] = (f32x4){0.f, 0.f, 0.f, 0.f};
;         for (int t = 0; t < nt - 2; t += 2) {
;             G_TILE(G_A0, G_B0, true, G_B1, G_A1, t + 1, true, t + 2, (void)0);
.LBB0_378:
	s_mov_b32 m0, s72
	s_add_i32 s25, s24, 0xffffff80
	ds_read_b64_tr_b16 v[170:171], v165
	ds_read_b64_tr_b16 v[172:173], v166
	ds_read_b64_tr_b16 v[176:177], v166 offset:32
	ds_read_b128 v[178:181], v162
	ds_read_b64_tr_b16 v[174:175], v165 offset:32
	ds_read_b64_tr_b16 v[182:183], v165 offset:64
	ds_read_b64_tr_b16 v[186:187], v165 offset:96
	ds_read_b64_tr_b16 v[184:185], v166 offset:64
	ds_read_b64_tr_b16 v[188:189], v166 offset:96
	ds_read_b128 v[190:193], v162 offset:2048
	ds_read_b128 v[198:201], v162 offset:4096
	buffer_load_dwordx4 v163, s[20:23], s25 offen lds
	s_mov_b32 m0, s71
	v_mfma_f32_16x16x32_bf16 v[44:47], v[244:247], v[252:255], v[44:47]
	v_mfma_f32_16x16x32_bf16 v[40:43], v[248:251], v[252:255], v[40:43]
	v_mfma_f32_16x16x32_bf16 v[36:39], v[202:205], v[252:255], v[36:39]
	v_mfma_f32_16x16x32_bf16 v[32:35], v[206:209], v[252:255], v[32:35]
	s_waitcnt lgkmcnt(7)
	v_mfma_f32_16x16x32_bf16 v[156:159], v[170:173], v[178:181], v[156:159]
	buffer_load_dwordx4 v164, s[20:23], s25 offen lds
	s_waitcnt lgkmcnt(6)
	v_mfma_f32_16x16x32_bf16 v[152:155], v[174:177], v[178:181], v[152:155]
	s_waitcnt lgkmcnt(3)
	v_mfma_f32_16x16x32_bf16 v[148:151], v[182:185], v[178:181], v[148:151]
	s_waitcnt lgkmcnt(2)
	v_mfma_f32_16x16x32_bf16 v[144:147], v[186:189], v[178:181], v[144:147]
	s_waitcnt lgkmcnt(1)
	v_mfma_f32_16x16x32_bf16 v[140:143], v[170:173], v[190:193], v[140:143]
	s_mov_b32 m0, s70
	s_nop 0
	buffer_load_dwordx4 v167, s[20:23], s25 offen lds
	ds_read_b128 v[178:181], v162 offset:6144
	s_waitcnt vmcnt(10)
	v_cvt_pk_bf16_f32 v15, v14, v15
	v_cvt_pk_bf16_f32 v14, v12, v13
	v_mfma_f32_16x16x32_bf16 v[136:139], v[174:177], v[190:193], v[136:139]
	ds_write_b64 v161, v[14:15] offset:34816
	v_mfma_f32_16x16x32_bf16 v[132:135], v[182:185], v[190:193], v[132:135]
	s_mov_b32 m0, s68
	s_nop 0
	buffer_load_dwordx4 v168, s[20:23], s25 offen lds
	s_add_i32 s25, s9, 0xfff20000
	v_mfma_f32_16x16x32_bf16 v[128:131], v[186:189], v[190:193], v[128:131]
	s_waitcnt lgkmcnt(2)
	v_mfma_f32_16x16x32_bf16 v[124:127], v[170:173], v[198:201], v[124:127]
	ds_read_b128 v[190:193], v162 offset:8192
	v_mfma_f32_16x16x32_bf16 v[120:123], v[174:177], v[198:201], v[120:123]
	v_mfma_f32_16x16x32_bf16 v[116:119], v[182:185], v[198:201], v[116:119]
	v_mfma_f32_16x16x32_bf16 v[112:115], v[186:189], v[198:201], v[112:115]
	s_waitcnt lgkmcnt(2)
	v_mfma_f32_16x16x32_bf16 v[108:111], v[170:173], v[178:181], v[108:111]
	ds_read_b128 v[198:201], v162 offset:10240
	buffer_load_dwordx4 v[12:15], v160, s[12:15], s25 offen
	s_waitcnt vmcnt(10)
	v_cvt_pk_bf16_f32 v31, v30, v31
	v_cvt_pk_bf16_f32 v30, v28, v29
	v_mfma_f32_16x16x32_bf16 v[104:107], v[174:177], v[178:181], v[104:107]
	ds_write_b64 v161, v[30:31] offset:43520
	v_mfma_f32_16x16x32_bf16 v[100:103], v[182:185], v[178:181], v[100:103]
	v_mfma_f32_16x16x32_bf16 v[96:99], v[186:189], v[178:181], v[96:99]
	s_add_i32 s26, s9, 0xfff40000
	s_waitcnt lgkmcnt(2)
	v_mfma_f32_16x16x32_bf16 v[92:95], v[170:173], v[190:193], v[92:95]
	ds_read_b128 v[178:181], v162 offset:12288
	v_mfma_f32_16x16x32_bf16 v[88:91], v[174:177], v[190:193], v[88:91]
	v_mfma_f32_16x16x32_bf16 v[84:87], v[182:185], v[190:193], v[84:87]
	v_mfma_f32_16x16x32_bf16 v[80:83], v[186:189], v[190:193], v[80:83]
	s_waitcnt lgkmcnt(2)
	v_mfma_f32_16x16x32_bf16 v[76:79], v[170:173], v[198:201], v[76:79]
	ds_read_b128 v[190:193], v162 offset:14336
	v_cvt_pk_bf16_f32 v7, v6, v7
	v_cvt_pk_bf16_f32 v6, v4, v5
	v_mfma_f32_16x16x32_bf16 v[72:75], v[174:177], v[198:201], v[72:75]
	ds_write_b64 v161, v[6:7] offset:52224
	v_mfma_f32_16x16x32_bf16 v[68:71], v[182:185], v[198:201], v[68:71]
	v_mfma_f32_16x16x32_bf16 v[64:67], v[186:189], v[198:201], v[64:67]
	s_add_i32 s27, s9, 0xfff60000
	buffer_load_dwordx4 v[28:31], v160, s[12:15], s26 offen
	s_waitcnt lgkmcnt(2)
	v_mfma_f32_16x16x32_bf16 v[60:63], v[170:173], v[178:181], v[60:63]
	ds_read_b128 v[198:201], v162 offset:1024
	v_mfma_f32_16x16x32_bf16 v[56:59], v[174:177], v[178:181], v[56:59]
	v_mfma_f32_16x16x32_bf16 v[52:55], v[182:185], v[178:181], v[52:55]
	v_mfma_f32_16x16x32_bf16 v[48:51], v[186:189], v[178:181], v[48:51]
	s_waitcnt lgkmcnt(2)
	v_mfma_f32_16x16x32_bf16 v[44:47], v[170:173], v[190:193], v[44:47]
	ds_read_b128 v[170:173], v162 offset:3072
	buffer_load_dwordx4 v[4:7], v160, s[12:15], s27 offen
	s_waitcnt vmcnt(11)
	v_cvt_pk_bf16_f32 v27, v26, v27
	v_cvt_pk_bf16_f32 v26, v24, v25
	v_mfma_f32_16x16x32_bf16 v[40:43], v[174:177], v[190:193], v[40:43]
	ds_read_b64_tr_b16 v[244:245], v165 offset:17408
	ds_read_b64_tr_b16 v[248:249], v165 offset:17440
	ds_read_b64_tr_b16 v[202:203], v165 offset:17472
	ds_read_b64_tr_b16 v[206:207], v165 offset:17504
	ds_read_b64_tr_b16 v[246:247], v166 offset:17408
	ds_read_b64_tr_b16 v[250:251], v166 offset:17440
	ds_read_b64_tr_b16 v[204:205], v166 offset:17472
	ds_read_b64_tr_b16 v[208:209], v166 offset:17504
	ds_write_b64 v161, v[26:27] offset:60928
	v_mfma_f32_16x16x32_bf16 v[36:39], v[182:185], v[190:193], v[36:39]
	v_mfma_f32_16x16x32_bf16 v[32:35], v[186:189], v[190:193], v[32:35]
	s_add_i32 s45, s9, 0xfff80000
	s_waitcnt lgkmcnt(4)
	v_mfma_f32_16x16x32_bf16 v[156:159], v[244:247], v[198:201], v[156:159]
	ds_read_b128 v[182:185], v162 offset:5120
	s_waitcnt lgkmcnt(4)
	v_mfma_f32_16x16x32_bf16 v[152:155], v[248:251], v[198:201], v[152:155]
	s_waitcnt lgkmcnt(3)
	v_mfma_f32_16x16x32_bf16 v[148:151], v[202:205], v[198:201], v[148:151]
	s_waitcnt lgkmcnt(2)
	v_mfma_f32_16x16x32_bf16 v[144:147], v[206:209], v[198:201], v[144:147]
	v_mfma_f32_16x16x32_bf16 v[140:143], v[244:247], v[170:173], v[140:143]
	ds_read_b128 v[186:189], v162 offset:7168
	buffer_load_dwordx4 v[24:27], v160, s[12:15], s45 offen
	s_waitcnt vmcnt(11)
; #define G_DMA_A(kt, AO) do { G_DMA1(kt, AO, 0); G_DMA1(kt, AO, 1); G_DMA1(kt, AO, 2); G_DMA1(kt, AO, 3); if (MF == 9) G_DMA5(kt, AO); } while (0)
; #define G_ISSUE_B(kt) do { const unsigned _sb = (unsigned)(kt) * 4u * kstepB; \
;         _Pragma("unroll") for (int _i = 0; _i < 8; ++_i) sb[_i] = bload16(_i < 4 ? rsB0 : rsB1, vob, _sb + (_i & 3) * kstepB); } while (0)
; #define G_WRITE_B(BO) do { \
;         _Pragma("unroll") for (int _i = 0; _i < 8; ++_i) *(LAS u32x2*)(b_wr + (BO) + (_i & 3) * (16 * G_BSTRIDE) + (_i >> 2) * SLAB1) = pack4(__builtin_bit_cast(f32x4, sb[_i])); } while (0)
; #define G_ENDTILE(VM) do { asm volatile("s_waitcnt vmcnt(" #VM ")" ::: "memory"); \
;         asm volatile("s_waitcnt lgkmcnt(0)" ::: "memory"); __builtin_amdgcn_s_barrier(); asm volatile("" ::: "memory"); } while (0)
;     ...
;     __builtin_amdgcn_s_barrier();
;     G_DMA_A(0, G_A0); G_ISSUE_B(0); G_WRITE_B(G_B0);
;     __builtin_amdgcn_sched_barrier(0);
;     G_ISSUE_B(1);
;     __builtin_amdgcn_sched_barrier(0);
;     G_ENDTILE(8);
;     for (int ui = 0;; ++ui) {
; #pragma unroll
;         for (int m = 0; m < MF; ++m)
; #pragma unroll
;             for (int n = 0; n < 4; ++n) acc[m][n] = (f32x4){0.f, 0.f, 0.f, 0.f};
;         for (int t = 0; t < nt - 2; t += 2) {
;             G_TILE(G_A0, G_B0, true, G_B1, G_A1, t + 1, true, t + 2, (void)0);
;             G_ENDTILE(8);
;             G_TILE(G_A1, G_B1, true, G_B0, G_A0, t + 2, true, t + 3, (void)0);
;             G_ENDTILE(8);
	v_cvt_pk_bf16_f32 v23, v22, v23
	v_cvt_pk_bf16_f32 v22, v20, v21
	v_mfma_f32_16x16x32_bf16 v[136:139], v[248:251], v[170:173], v[136:139]
	ds_write_b64 v161, v[22:23] offset:35072
	v_mfma_f32_16x16x32_bf16 v[132:135], v[202:205], v[170:173], v[132:135]
	v_mfma_f32_16x16x32_bf16 v[128:131], v[206:209], v[170:173], v[128:131]
	s_waitcnt lgkmcnt(2)
	v_mfma_f32_16x16x32_bf16 v[124:127], v[244:247], v[182:185], v[124:127]
	ds_read_b128 v[170:173], v162 offset:9216
	v_mfma_f32_16x16x32_bf16 v[120:123], v[248:251], v[182:185], v[120:123]
	v_mfma_f32_16x16x32_bf16 v[116:119], v[202:205], v[182:185], v[116:119]
	v_mfma_f32_16x16x32_bf16 v[112:115], v[206:209], v[182:185], v[112:115]
	s_waitcnt lgkmcnt(2)
	v_mfma_f32_16x16x32_bf16 v[108:111], v[244:247], v[186:189], v[108:111]
	ds_read_b128 v[182:185], v162 offset:11264
	buffer_load_dwordx4 v[20:23], v160, s[16:19], s25 offen
	s_waitcnt vmcnt(10)
	v_cvt_pk_bf16_f32 v11, v10, v11
	v_cvt_pk_bf16_f32 v10, v8, v9
	v_mfma_f32_16x16x32_bf16 v[104:107], v[248:251], v[186:189], v[104:107]
	ds_write_b64 v161, v[10:11] offset:43776
	v_mfma_f32_16x16x32_bf16 v[100:103], v[202:205], v[186:189], v[100:103]
	v_mfma_f32_16x16x32_bf16 v[96:99], v[206:209], v[186:189], v[96:99]
	s_waitcnt lgkmcnt(2)
	v_mfma_f32_16x16x32_bf16 v[92:95], v[244:247], v[170:173], v[92:95]
	ds_read_b128 v[186:189], v162 offset:13312
	v_mfma_f32_16x16x32_bf16 v[88:91], v[248:251], v[170:173], v[88:91]
	v_mfma_f32_16x16x32_bf16 v[84:87], v[202:205], v[170:173], v[84:87]
	v_mfma_f32_16x16x32_bf16 v[80:83], v[206:209], v[170:173], v[80:83]
	s_waitcnt lgkmcnt(2)
	v_mfma_f32_16x16x32_bf16 v[76:79], v[244:247], v[182:185], v[76:79]
	ds_read_b128 v[252:255], v162 offset:15360
	v_cvt_pk_bf16_f32 v3, v2, v3
	v_cvt_pk_bf16_f32 v2, v0, v1
	v_mfma_f32_16x16x32_bf16 v[72:75], v[248:251], v[182:185], v[72:75]
	ds_write_b64 v161, v[2:3] offset:52480
	v_mfma_f32_16x16x32_bf16 v[68:71], v[202:205], v[182:185], v[68:71]
	v_mfma_f32_16x16x32_bf16 v[64:67], v[206:209], v[182:185], v[64:67]
	buffer_load_dwordx4 v[8:11], v160, s[16:19], s26 offen
	s_waitcnt lgkmcnt(2)
	v_mfma_f32_16x16x32_bf16 v[60:63], v[244:247], v[186:189], v[60:63]
	buffer_load_dwordx4 v[0:3], v160, s[16:19], s27 offen
	s_waitcnt vmcnt(11)
	v_cvt_pk_bf16_f32 v19, v18, v19
	v_cvt_pk_bf16_f32 v18, v16, v17
	v_mfma_f32_16x16x32_bf16 v[56:59], v[248:251], v[186:189], v[56:59]
	ds_write_b64 v161, v[18:19] offset:61184
	v_mfma_f32_16x16x32_bf16 v[52:55], v[202:205], v[186:189], v[52:55]
	buffer_load_dwordx4 v[16:19], v160, s[16:19], s45 offen
	v_mfma_f32_16x16x32_bf16 v[48:51], v[206:209], v[186:189], v[48:51]
	s_waitcnt vmcnt(8)
	s_mov_b32 m0, s59
	s_waitcnt lgkmcnt(0)
	s_barrier
	ds_read_b64_tr_b16 v[170:171], v165 offset:34816
	ds_read_b64_tr_b16 v[172:173], v166 offset:34816
	ds_read_b64_tr_b16 v[176:177], v166 offset:34848
	ds_read_b128 v[178:181], v162 offset:32768
	ds_read_b64_tr_b16 v[174:175], v165 offset:34848
	ds_read_b64_tr_b16 v[182:183], v165 offset:34880
	ds_read_b64_tr_b16 v[186:187], v165 offset:34912
	ds_read_b64_tr_b16 v[184:185], v166 offset:34880
	ds_read_b64_tr_b16 v[188:189], v166 offset:34912
	ds_read_b128 v[190:193], v162 offset:34816
	ds_read_b128 v[198:201], v162 offset:36864
	buffer_load_dwordx4 v163, s[20:23], s24 offen lds
	s_mov_b32 m0, s60
	v_mfma_f32_16x16x32_bf16 v[44:47], v[244:247], v[252:255], v[44:47]
	v_mfma_f32_16x16x32_bf16 v[40:43], v[248:251], v[252:255], v[40:43]
	v_mfma_f32_16x16x32_bf16 v[36:39], v[202:205], v[252:255], v[36:39]
	v_mfma_f32_16x16x32_bf16 v[32:35], v[206:209], v[252:255], v[32:35]
	s_waitcnt lgkmcnt(7)
	v_mfma_f32_16x16x32_bf16 v[156:159], v[170:173], v[178:181], v[156:159]
	buffer_load_dwordx4 v164, s[20:23], s24 offen lds
	s_add_i32 s25, s9, 0xfffa0000
	s_waitcnt lgkmcnt(6)
	v_mfma_f32_16x16x32_bf16 v[152:155], v[174:177], v[178:181], v[152:155]
	s_waitcnt lgkmcnt(3)
	v_mfma_f32_16x16x32_bf16 v[148:151], v[182:185], v[178:181], v[148:151]
	s_waitcnt lgkmcnt(2)
	v_mfma_f32_16x16x32_bf16 v[144:147], v[186:189], v[178:181], v[144:147]
	s_waitcnt lgkmcnt(1)
	v_mfma_f32_16x16x32_bf16 v[140:143], v[170:173], v[190:193], v[140:143]
	s_mov_b32 m0, s61
	s_nop 0
	buffer_load_dwordx4 v167, s[20:23], s24 offen lds
	ds_read_b128 v[178:181], v162 offset:38912
	s_waitcnt vmcnt(10)
	v_cvt_pk_bf16_f32 v15, v14, v15
	v_cvt_pk_bf16_f32 v14, v12, v13
	v_mfma_f32_16x16x32_bf16 v[136:139], v[174:177], v[190:193], v[136:139]
	ds_write_b64 v161, v[14:15]
	v_mfma_f32_16x16x32_bf16 v[132:135], v[182:185], v[190:193], v[132:135]
	s_mov_b32 m0, s62
	s_nop 0
	buffer_load_dwordx4 v168, s[20:23], s24 offen lds
	v_mfma_f32_16x16x32_bf16 v[128:131], v[186:189], v[190:193], v[128:131]
	s_waitcnt lgkmcnt(2)
	v_mfma_f32_16x16x32_bf16 v[124:127], v[170:173], v[198:201], v[124:127]
	ds_read_b128 v[190:193], v162 offset:40960
	v_mfma_f32_16x16x32_bf16 v[120:123], v[174:177], v[198:201], v[120:123]
	v_mfma_f32_16x16x32_bf16 v[116:119], v[182:185], v[198:201], v[116:119]
	v_mfma_f32_16x16x32_bf16 v[112:115], v[186:189], v[198:201], v[112:115]
	s_waitcnt lgkmcnt(2)
	v_mfma_f32_16x16x32_bf16 v[108:111], v[170:173], v[178:181], v[108:111]
	ds_read_b128 v[198:201], v162 offset:43008
	buffer_load_dwordx4 v[12:15], v160, s[12:15], s25 offen
	s_waitcnt vmcnt(11)
	v_cvt_pk_bf16_f32 v31, v30, v31
	v_cvt_pk_bf16_f32 v30, v28, v29
	v_mfma_f32_16x16x32_bf16 v[104:107], v[174:177], v[178:181], v[104:107]
	ds_write_b64 v161, v[30:31] offset:8704
	v_mfma_f32_16x16x32_bf16 v[100:103], v[182:185], v[178:181], v[100:103]
	v_mfma_f32_16x16x32_bf16 v[96:99], v[186:189], v[178:181], v[96:99]
	s_add_i32 s26, s9, 0xfffc0000
	s_waitcnt lgkmcnt(2)
; #define G_DMA_A(kt, AO) do { G_DMA1(kt, AO, 0); G_DMA1(kt, AO, 1); G_DMA1(kt, AO, 2); G_DMA1(kt, AO, 3); if (MF == 9) G_DMA5(kt, AO); } while (0)
; #define G_ISSUE_B(kt) do { const unsigned _sb = (unsigned)(kt) * 4u * kstepB; \
;         _Pragma("unroll") for (int _i = 0; _i < 8; ++_i) sb[_i] = bload16(_i < 4 ? rsB0 : rsB1, vob, _sb + (_i & 3) * kstepB); } while (0)
; #define G_WRITE_B(BO) do { \
;         _Pragma("unroll") for (int _i = 0; _i < 8; ++_i) *(LAS u32x2*)(b_wr + (BO) + (_i & 3) * (16 * G_BSTRIDE) + (_i >> 2) * SLAB1) = pack4(__builtin_bit_cast(f32x4, sb[_i])); } while (0)
; #define G_ENDTILE(VM) do { asm volatile("s_waitcnt vmcnt(" #VM ")" ::: "memory"); \
;         asm volatile("s_waitcnt lgkmcnt(0)" ::: "memory"); __builtin_amdgcn_s_barrier(); asm volatile("" ::: "memory"); } while (0)
;     ...
;     __builtin_amdgcn_s_barrier();
;     G_DMA_A(0, G_A0); G_ISSUE_B(0); G_WRITE_B(G_B0);
;     __builtin_amdgcn_sched_barrier(0);
;     G_ISSUE_B(1);
;     __builtin_amdgcn_sched_barrier(0);
;     G_ENDTILE(8);
;     for (int ui = 0;; ++ui) {
; #pragma unroll
;         for (int m = 0; m < MF; ++m)
; #pragma unroll
;             for (int n = 0; n < 4; ++n) acc[m][n] = (f32x4){0.f, 0.f, 0.f, 0.f};
;         for (int t = 0; t < nt - 2; t += 2) {
;             G_TILE(G_A0, G_B0, true, G_B1, G_A1, t + 1, true, t + 2, (void)0);
;             G_ENDTILE(8);
;             G_TILE(G_A1, G_B1, true, G_B0, G_A0, t + 2, true, t + 3, (void)0);
;             G_ENDTILE(8);
;         }
	v_mfma_f32_16x16x32_bf16 v[92:95], v[170:173], v[190:193], v[92:95]
	ds_read_b128 v[178:181], v162 offset:45056
	v_mfma_f32_16x16x32_bf16 v[88:91], v[174:177], v[190:193], v[88:91]
	v_mfma_f32_16x16x32_bf16 v[84:87], v[182:185], v[190:193], v[84:87]
	v_mfma_f32_16x16x32_bf16 v[80:83], v[186:189], v[190:193], v[80:83]
	s_waitcnt lgkmcnt(2)
	v_mfma_f32_16x16x32_bf16 v[76:79], v[170:173], v[198:201], v[76:79]
	ds_read_b128 v[190:193], v162 offset:47104
	buffer_load_dwordx4 v[28:31], v160, s[12:15], s26 offen
	s_waitcnt vmcnt(11)
	v_cvt_pk_bf16_f32 v7, v6, v7
	v_cvt_pk_bf16_f32 v6, v4, v5
	v_mfma_f32_16x16x32_bf16 v[72:75], v[174:177], v[198:201], v[72:75]
	ds_write_b64 v161, v[6:7] offset:17408
	v_mfma_f32_16x16x32_bf16 v[68:71], v[182:185], v[198:201], v[68:71]
	v_mfma_f32_16x16x32_bf16 v[64:67], v[186:189], v[198:201], v[64:67]
	s_add_i32 s27, s9, 0xfffe0000
	s_waitcnt lgkmcnt(2)
	v_mfma_f32_16x16x32_bf16 v[60:63], v[170:173], v[178:181], v[60:63]
	ds_read_b128 v[198:201], v162 offset:33792
	v_mfma_f32_16x16x32_bf16 v[56:59], v[174:177], v[178:181], v[56:59]
	v_mfma_f32_16x16x32_bf16 v[52:55], v[182:185], v[178:181], v[52:55]
	v_mfma_f32_16x16x32_bf16 v[48:51], v[186:189], v[178:181], v[48:51]
	s_waitcnt lgkmcnt(2)
	v_mfma_f32_16x16x32_bf16 v[44:47], v[170:173], v[190:193], v[44:47]
	ds_read_b128 v[170:173], v162 offset:35840
	buffer_load_dwordx4 v[4:7], v160, s[12:15], s27 offen
	s_waitcnt vmcnt(11)
	v_cvt_pk_bf16_f32 v27, v26, v27
	v_cvt_pk_bf16_f32 v26, v24, v25
	v_mfma_f32_16x16x32_bf16 v[40:43], v[174:177], v[190:193], v[40:43]
	ds_read_b64_tr_b16 v[244:245], v165 offset:52224
	ds_read_b64_tr_b16 v[248:249], v165 offset:52256
	ds_read_b64_tr_b16 v[202:203], v165 offset:52288
	ds_read_b64_tr_b16 v[206:207], v165 offset:52320
	ds_read_b64_tr_b16 v[246:247], v166 offset:52224
	ds_read_b64_tr_b16 v[250:251], v166 offset:52256
	ds_read_b64_tr_b16 v[204:205], v166 offset:52288
	ds_read_b64_tr_b16 v[208:209], v166 offset:52320
	ds_write_b64 v161, v[26:27] offset:26112
	v_mfma_f32_16x16x32_bf16 v[36:39], v[182:185], v[190:193], v[36:39]
	v_mfma_f32_16x16x32_bf16 v[32:35], v[186:189], v[190:193], v[32:35]
	s_waitcnt lgkmcnt(4)
	v_mfma_f32_16x16x32_bf16 v[156:159], v[244:247], v[198:201], v[156:159]
	ds_read_b128 v[182:185], v162 offset:37888
	s_waitcnt lgkmcnt(4)
	v_mfma_f32_16x16x32_bf16 v[152:155], v[248:251], v[198:201], v[152:155]
	s_waitcnt lgkmcnt(3)
	v_mfma_f32_16x16x32_bf16 v[148:151], v[202:205], v[198:201], v[148:151]
	s_waitcnt lgkmcnt(2)
	v_mfma_f32_16x16x32_bf16 v[144:147], v[206:209], v[198:201], v[144:147]
	v_mfma_f32_16x16x32_bf16 v[140:143], v[244:247], v[170:173], v[140:143]
	ds_read_b128 v[186:189], v162 offset:39936
	buffer_load_dwordx4 v[24:27], v160, s[12:15], s9 offen
	s_waitcnt vmcnt(11)
	v_cvt_pk_bf16_f32 v23, v22, v23
	v_cvt_pk_bf16_f32 v22, v20, v21
	v_mfma_f32_16x16x32_bf16 v[136:139], v[248:251], v[170:173], v[136:139]
	ds_write_b64 v161, v[22:23] offset:256
	v_mfma_f32_16x16x32_bf16 v[132:135], v[202:205], v[170:173], v[132:135]
	v_mfma_f32_16x16x32_bf16 v[128:131], v[206:209], v[170:173], v[128:131]
	s_waitcnt lgkmcnt(2)
	v_mfma_f32_16x16x32_bf16 v[124:127], v[244:247], v[182:185], v[124:127]
	ds_read_b128 v[170:173], v162 offset:41984
	v_mfma_f32_16x16x32_bf16 v[120:123], v[248:251], v[182:185], v[120:123]
	v_mfma_f32_16x16x32_bf16 v[116:119], v[202:205], v[182:185], v[116:119]
	v_mfma_f32_16x16x32_bf16 v[112:115], v[206:209], v[182:185], v[112:115]
	s_waitcnt lgkmcnt(2)
	v_mfma_f32_16x16x32_bf16 v[108:111], v[244:247], v[186:189], v[108:111]
	ds_read_b128 v[182:185], v162 offset:44032
	buffer_load_dwordx4 v[20:23], v160, s[16:19], s25 offen
	s_waitcnt vmcnt(11)
	v_cvt_pk_bf16_f32 v11, v10, v11
	v_cvt_pk_bf16_f32 v10, v8, v9
	v_mfma_f32_16x16x32_bf16 v[104:107], v[248:251], v[186:189], v[104:107]
	ds_write_b64 v161, v[10:11] offset:8960
	v_mfma_f32_16x16x32_bf16 v[100:103], v[202:205], v[186:189], v[100:103]
	v_mfma_f32_16x16x32_bf16 v[96:99], v[206:209], v[186:189], v[96:99]
	s_waitcnt lgkmcnt(2)
	v_mfma_f32_16x16x32_bf16 v[92:95], v[244:247], v[170:173], v[92:95]
	ds_read_b128 v[186:189], v162 offset:46080
	v_mfma_f32_16x16x32_bf16 v[88:91], v[248:251], v[170:173], v[88:91]
	v_mfma_f32_16x16x32_bf16 v[84:87], v[202:205], v[170:173], v[84:87]
	v_mfma_f32_16x16x32_bf16 v[80:83], v[206:209], v[170:173], v[80:83]
	s_waitcnt lgkmcnt(2)
	v_mfma_f32_16x16x32_bf16 v[76:79], v[244:247], v[182:185], v[76:79]
	ds_read_b128 v[252:255], v162 offset:48128
	buffer_load_dwordx4 v[8:11], v160, s[16:19], s26 offen
	s_waitcnt vmcnt(11)
	v_cvt_pk_bf16_f32 v3, v2, v3
	v_cvt_pk_bf16_f32 v2, v0, v1
	v_mfma_f32_16x16x32_bf16 v[72:75], v[248:251], v[182:185], v[72:75]
	ds_write_b64 v161, v[2:3] offset:17664
	v_mfma_f32_16x16x32_bf16 v[68:71], v[202:205], v[182:185], v[68:71]
	v_mfma_f32_16x16x32_bf16 v[64:67], v[206:209], v[182:185], v[64:67]
	s_waitcnt lgkmcnt(2)
	v_mfma_f32_16x16x32_bf16 v[60:63], v[244:247], v[186:189], v[60:63]
	buffer_load_dwordx4 v[0:3], v160, s[16:19], s27 offen
	s_waitcnt vmcnt(11)
	v_cvt_pk_bf16_f32 v19, v18, v19
	v_cvt_pk_bf16_f32 v18, v16, v17
	v_mfma_f32_16x16x32_bf16 v[56:59], v[248:251], v[186:189], v[56:59]
	ds_write_b64 v161, v[18:19] offset:26368
	v_mfma_f32_16x16x32_bf16 v[52:55], v[202:205], v[186:189], v[52:55]
	buffer_load_dwordx4 v[16:19], v160, s[16:19], s9 offen
	v_mfma_f32_16x16x32_bf16 v[48:51], v[206:209], v[186:189], v[48:51]
	s_waitcnt vmcnt(8)
	s_waitcnt lgkmcnt(0)
	s_barrier
	s_add_i32 s8, s8, 2
	s_add_i32 s9, s9, 0x100000
	s_addk_i32 s24, 0x100
	s_cmp_ge_i32 s8, s67
	s_cbranch_scc0 .LBB0_378
	v_mfma_f32_16x16x32_bf16 v[44:47], v[244:247], v[252:255], v[44:47]
	v_mfma_f32_16x16x32_bf16 v[40:43], v[248:251], v[252:255], v[40:43]
	v_mfma_f32_16x16x32_bf16 v[36:39], v[202:205], v[252:255], v[36:39]
	v_mfma_f32_16x16x32_bf16 v[32:35], v[206:209], v[252:255], v[32:35]
	s_branch .LBB0_380

; #define G_DMA_A(kt, AO) do { G_DMA1(kt, AO, 0); G_DMA1(kt, AO, 1); G_DMA1(kt, AO, 2); G_DMA1(kt, AO, 3); if (MF == 9) G_DMA5(kt, AO); } while (0)
; #define G_ISSUE_B(kt) do { const unsigned _sb = (unsigned)(kt) * 4u * kstepB; \
;         _Pragma("unroll") for (int _i = 0; _i < 8; ++_i) sb[_i] = bload16(_i < 4 ? rsB0 : rsB1, vob, _sb + (_i & 3) * kstepB); } while (0)
; #define G_WRITE_B(BO) do { \
;         _Pragma("unroll") for (int _i = 0; _i < 8; ++_i) *(LAS u32x2*)(b_wr + (BO) + (_i & 3) * (16 * G_BSTRIDE) + (_i >> 2) * SLAB1) = pack4(__builtin_bit_cast(f32x4, sb[_i])); } while (0)
; #define G_ENDTILE(VM) do { asm volatile("s_waitcnt vmcnt(" #VM ")" ::: "memory"); \
;         asm volatile("s_waitcnt lgkmcnt(0)" ::: "memory"); __builtin_amdgcn_s_barrier(); asm volatile("" ::: "memory"); } while (0)
;     ...
;     __builtin_amdgcn_s_barrier();
;     G_DMA_A(0, G_A0); G_ISSUE_B(0); G_WRITE_B(G_B0);
;     __builtin_amdgcn_sched_barrier(0);
;     G_ISSUE_B(1);
;     __builtin_amdgcn_sched_barrier(0);
;     G_ENDTILE(8);
;     for (int ui = 0;; ++ui) {
; #pragma unroll
;         for (int m = 0; m < MF; ++m)
; #pragma unroll
;             for (int n = 0; n < 4; ++n) acc[m][n] = (f32x4){0.f, 0.f, 0.f, 0.f};
;         for (int t = 0; t < nt - 2; t += 2) {
;             G_TILE(G_A0, G_B0, true, G_B1, G_A1, t + 1, true, t + 2, (void)0);
.LBB0_899:
	s_mov_b32 m0, s64
	s_add_i32 s69, s45, 0xffffff80
	ds_read_b64_tr_b16 v[170:171], v166
	ds_read_b64_tr_b16 v[172:173], v167
	ds_read_b64_tr_b16 v[176:177], v167 offset:32
	ds_read_b128 v[178:181], v162
	ds_read_b64_tr_b16 v[174:175], v166 offset:32
	ds_read_b64_tr_b16 v[182:183], v166 offset:64
	ds_read_b64_tr_b16 v[186:187], v166 offset:96
	ds_read_b64_tr_b16 v[184:185], v167 offset:64
	ds_read_b64_tr_b16 v[188:189], v167 offset:96
	ds_read_b128 v[190:193], v162 offset:2048
	ds_read_b128 v[198:201], v162 offset:4096
	buffer_load_dwordx4 v163, s[20:23], s69 offen lds
	s_mov_b32 m0, s63
	v_mfma_f32_16x16x32_bf16 v[44:47], v[244:247], v[252:255], v[44:47]
	v_mfma_f32_16x16x32_bf16 v[40:43], v[248:251], v[252:255], v[40:43]
	v_mfma_f32_16x16x32_bf16 v[36:39], v[202:205], v[252:255], v[36:39]
	v_mfma_f32_16x16x32_bf16 v[32:35], v[206:209], v[252:255], v[32:35]
	s_waitcnt lgkmcnt(7)
	v_mfma_f32_16x16x32_bf16 v[156:159], v[170:173], v[178:181], v[156:159]
	buffer_load_dwordx4 v165, s[20:23], s69 offen lds
	s_waitcnt lgkmcnt(6)
	v_mfma_f32_16x16x32_bf16 v[152:155], v[174:177], v[178:181], v[152:155]
	s_waitcnt lgkmcnt(3)
	v_mfma_f32_16x16x32_bf16 v[148:151], v[182:185], v[178:181], v[148:151]
	s_waitcnt lgkmcnt(2)
	v_mfma_f32_16x16x32_bf16 v[144:147], v[186:189], v[178:181], v[144:147]
	s_waitcnt lgkmcnt(1)
	v_mfma_f32_16x16x32_bf16 v[140:143], v[170:173], v[190:193], v[140:143]
	s_mov_b32 m0, s62
	s_nop 0
	buffer_load_dwordx4 v164, s[20:23], s69 offen lds
	ds_read_b128 v[178:181], v162 offset:6144
	s_waitcnt vmcnt(10)
	v_cvt_pk_bf16_f32 v15, v14, v15
	v_cvt_pk_bf16_f32 v14, v12, v13
	v_mfma_f32_16x16x32_bf16 v[136:139], v[174:177], v[190:193], v[136:139]
	ds_write_b64 v161, v[14:15] offset:34816
	v_mfma_f32_16x16x32_bf16 v[132:135], v[182:185], v[190:193], v[132:135]
	s_mov_b32 m0, s31
	s_nop 0
	buffer_load_dwordx4 v168, s[20:23], s69 offen lds
	s_add_i32 s69, s13, 0xfff20000
	v_mfma_f32_16x16x32_bf16 v[128:131], v[186:189], v[190:193], v[128:131]
	s_waitcnt lgkmcnt(2)
	v_mfma_f32_16x16x32_bf16 v[124:127], v[170:173], v[198:201], v[124:127]
	ds_read_b128 v[190:193], v162 offset:8192
	v_mfma_f32_16x16x32_bf16 v[120:123], v[174:177], v[198:201], v[120:123]
	v_mfma_f32_16x16x32_bf16 v[116:119], v[182:185], v[198:201], v[116:119]
	v_mfma_f32_16x16x32_bf16 v[112:115], v[186:189], v[198:201], v[112:115]
	s_waitcnt lgkmcnt(2)
	v_mfma_f32_16x16x32_bf16 v[108:111], v[170:173], v[178:181], v[108:111]
	ds_read_b128 v[198:201], v162 offset:10240
	buffer_load_dwordx4 v[12:15], v160, s[24:27], s69 offen
	s_waitcnt vmcnt(11)
	v_cvt_pk_bf16_f32 v3, v2, v3
	v_cvt_pk_bf16_f32 v2, v0, v1
	v_mfma_f32_16x16x32_bf16 v[104:107], v[174:177], v[178:181], v[104:107]
	ds_write_b64 v161, v[2:3] offset:43520
	v_mfma_f32_16x16x32_bf16 v[100:103], v[182:185], v[178:181], v[100:103]
	v_mfma_f32_16x16x32_bf16 v[96:99], v[186:189], v[178:181], v[96:99]
	s_add_i32 s74, s13, 0xfff40000
	s_waitcnt lgkmcnt(2)
	v_mfma_f32_16x16x32_bf16 v[92:95], v[170:173], v[190:193], v[92:95]
	ds_read_b128 v[178:181], v162 offset:12288
	v_mfma_f32_16x16x32_bf16 v[88:91], v[174:177], v[190:193], v[88:91]
	v_mfma_f32_16x16x32_bf16 v[84:87], v[182:185], v[190:193], v[84:87]
	v_mfma_f32_16x16x32_bf16 v[80:83], v[186:189], v[190:193], v[80:83]
	s_waitcnt lgkmcnt(2)
	v_mfma_f32_16x16x32_bf16 v[76:79], v[170:173], v[198:201], v[76:79]
	ds_read_b128 v[190:193], v162 offset:14336
	buffer_load_dwordx4 v[0:3], v160, s[24:27], s74 offen
	s_waitcnt vmcnt(11)
	v_cvt_pk_bf16_f32 v31, v30, v31
	v_cvt_pk_bf16_f32 v30, v28, v29
	v_mfma_f32_16x16x32_bf16 v[72:75], v[174:177], v[198:201], v[72:75]
	ds_write_b64 v161, v[30:31] offset:52224
	v_mfma_f32_16x16x32_bf16 v[68:71], v[182:185], v[198:201], v[68:71]
	v_mfma_f32_16x16x32_bf16 v[64:67], v[186:189], v[198:201], v[64:67]
	s_add_i32 s75, s13, 0xfff60000
	s_waitcnt lgkmcnt(2)
	v_mfma_f32_16x16x32_bf16 v[60:63], v[170:173], v[178:181], v[60:63]
	ds_read_b128 v[198:201], v162 offset:1024
	v_mfma_f32_16x16x32_bf16 v[56:59], v[174:177], v[178:181], v[56:59]
	v_mfma_f32_16x16x32_bf16 v[52:55], v[182:185], v[178:181], v[52:55]
	v_mfma_f32_16x16x32_bf16 v[48:51], v[186:189], v[178:181], v[48:51]
	s_waitcnt lgkmcnt(2)
	v_mfma_f32_16x16x32_bf16 v[44:47], v[170:173], v[190:193], v[44:47]
	ds_read_b128 v[170:173], v162 offset:3072
	buffer_load_dwordx4 v[28:31], v160, s[24:27], s75 offen
	s_waitcnt vmcnt(11)
	v_cvt_pk_bf16_f32 v27, v26, v27
	v_cvt_pk_bf16_f32 v26, v24, v25
	v_mfma_f32_16x16x32_bf16 v[40:43], v[174:177], v[190:193], v[40:43]
	ds_read_b64_tr_b16 v[244:245], v166 offset:17408
	ds_read_b64_tr_b16 v[248:249], v166 offset:17440
	ds_read_b64_tr_b16 v[202:203], v166 offset:17472
	ds_read_b64_tr_b16 v[206:207], v166 offset:17504
	ds_read_b64_tr_b16 v[246:247], v167 offset:17408
	ds_read_b64_tr_b16 v[250:251], v167 offset:17440
	ds_read_b64_tr_b16 v[204:205], v167 offset:17472
	ds_read_b64_tr_b16 v[208:209], v167 offset:17504
	ds_write_b64 v161, v[26:27] offset:60928
	v_mfma_f32_16x16x32_bf16 v[36:39], v[182:185], v[190:193], v[36:39]
	v_mfma_f32_16x16x32_bf16 v[32:35], v[186:189], v[190:193], v[32:35]
	s_add_i32 s76, s13, 0xfff80000
	s_waitcnt lgkmcnt(4)
	v_mfma_f32_16x16x32_bf16 v[156:159], v[244:247], v[198:201], v[156:159]
	ds_read_b128 v[182:185], v162 offset:5120
	s_waitcnt lgkmcnt(4)
	v_mfma_f32_16x16x32_bf16 v[152:155], v[248:251], v[198:201], v[152:155]
	s_waitcnt lgkmcnt(3)
	v_mfma_f32_16x16x32_bf16 v[148:151], v[202:205], v[198:201], v[148:151]
	s_waitcnt lgkmcnt(2)
	v_mfma_f32_16x16x32_bf16 v[144:147], v[206:209], v[198:201], v[144:147]
	v_mfma_f32_16x16x32_bf16 v[140:143], v[244:247], v[170:173], v[140:143]
	ds_read_b128 v[186:189], v162 offset:7168
	buffer_load_dwordx4 v[24:27], v160, s[24:27], s76 offen
	s_waitcnt vmcnt(11)
; #define G_DMA_A(kt, AO) do { G_DMA1(kt, AO, 0); G_DMA1(kt, AO, 1); G_DMA1(kt, AO, 2); G_DMA1(kt, AO, 3); if (MF == 9) G_DMA5(kt, AO); } while (0)
; #define G_ISSUE_B(kt) do { const unsigned _sb = (unsigned)(kt) * 4u * kstepB; \
;         _Pragma("unroll") for (int _i = 0; _i < 8; ++_i) sb[_i] = bload16(_i < 4 ? rsB0 : rsB1, vob, _sb + (_i & 3) * kstepB); } while (0)
; #define G_WRITE_B(BO) do { \
;         _Pragma("unroll") for (int _i = 0; _i < 8; ++_i) *(LAS u32x2*)(b_wr + (BO) + (_i & 3) * (16 * G_BSTRIDE) + (_i >> 2) * SLAB1) = pack4(__builtin_bit_cast(f32x4, sb[_i])); } while (0)
; #define G_ENDTILE(VM) do { asm volatile("s_waitcnt vmcnt(" #VM ")" ::: "memory"); \
;         asm volatile("s_waitcnt lgkmcnt(0)" ::: "memory"); __builtin_amdgcn_s_barrier(); asm volatile("" ::: "memory"); } while (0)
;     ...
;     __builtin_amdgcn_s_barrier();
;     G_DMA_A(0, G_A0); G_ISSUE_B(0); G_WRITE_B(G_B0);
;     __builtin_amdgcn_sched_barrier(0);
;     G_ISSUE_B(1);
;     __builtin_amdgcn_sched_barrier(0);
;     G_ENDTILE(8);
;     for (int ui = 0;; ++ui) {
; #pragma unroll
;         for (int m = 0; m < MF; ++m)
; #pragma unroll
;             for (int n = 0; n < 4; ++n) acc[m][n] = (f32x4){0.f, 0.f, 0.f, 0.f};
;         for (int t = 0; t < nt - 2; t += 2) {
;             G_TILE(G_A0, G_B0, true, G_B1, G_A1, t + 1, true, t + 2, (void)0);
;             G_ENDTILE(8);
;             G_TILE(G_A1, G_B1, true, G_B0, G_A0, t + 2, true, t + 3, (void)0);
;             G_ENDTILE(8);
	v_cvt_pk_bf16_f32 v23, v22, v23
	v_cvt_pk_bf16_f32 v22, v20, v21
	v_mfma_f32_16x16x32_bf16 v[136:139], v[248:251], v[170:173], v[136:139]
	ds_write_b64 v161, v[22:23] offset:35072
	v_mfma_f32_16x16x32_bf16 v[132:135], v[202:205], v[170:173], v[132:135]
	v_mfma_f32_16x16x32_bf16 v[128:131], v[206:209], v[170:173], v[128:131]
	s_waitcnt lgkmcnt(2)
	v_mfma_f32_16x16x32_bf16 v[124:127], v[244:247], v[182:185], v[124:127]
	ds_read_b128 v[170:173], v162 offset:9216
	v_mfma_f32_16x16x32_bf16 v[120:123], v[248:251], v[182:185], v[120:123]
	v_mfma_f32_16x16x32_bf16 v[116:119], v[202:205], v[182:185], v[116:119]
	v_mfma_f32_16x16x32_bf16 v[112:115], v[206:209], v[182:185], v[112:115]
	s_waitcnt lgkmcnt(2)
	v_mfma_f32_16x16x32_bf16 v[108:111], v[244:247], v[186:189], v[108:111]
	ds_read_b128 v[182:185], v162 offset:11264
	buffer_load_dwordx4 v[20:23], v160, s[16:19], s69 offen
	s_waitcnt vmcnt(11)
	v_cvt_pk_bf16_f32 v7, v6, v7
	v_cvt_pk_bf16_f32 v6, v4, v5
	v_mfma_f32_16x16x32_bf16 v[104:107], v[248:251], v[186:189], v[104:107]
	ds_write_b64 v161, v[6:7] offset:43776
	v_mfma_f32_16x16x32_bf16 v[100:103], v[202:205], v[186:189], v[100:103]
	v_mfma_f32_16x16x32_bf16 v[96:99], v[206:209], v[186:189], v[96:99]
	s_waitcnt lgkmcnt(2)
	v_mfma_f32_16x16x32_bf16 v[92:95], v[244:247], v[170:173], v[92:95]
	ds_read_b128 v[186:189], v162 offset:13312
	v_mfma_f32_16x16x32_bf16 v[88:91], v[248:251], v[170:173], v[88:91]
	v_mfma_f32_16x16x32_bf16 v[84:87], v[202:205], v[170:173], v[84:87]
	v_mfma_f32_16x16x32_bf16 v[80:83], v[206:209], v[170:173], v[80:83]
	s_waitcnt lgkmcnt(2)
	v_mfma_f32_16x16x32_bf16 v[76:79], v[244:247], v[182:185], v[76:79]
	ds_read_b128 v[252:255], v162 offset:15360
	buffer_load_dwordx4 v[4:7], v160, s[16:19], s74 offen
	s_waitcnt vmcnt(11)
	v_cvt_pk_bf16_f32 v11, v10, v11
	v_cvt_pk_bf16_f32 v10, v8, v9
	v_mfma_f32_16x16x32_bf16 v[72:75], v[248:251], v[182:185], v[72:75]
	ds_write_b64 v161, v[10:11] offset:52480
	v_mfma_f32_16x16x32_bf16 v[68:71], v[202:205], v[182:185], v[68:71]
	v_mfma_f32_16x16x32_bf16 v[64:67], v[206:209], v[182:185], v[64:67]
	s_waitcnt lgkmcnt(2)
	v_mfma_f32_16x16x32_bf16 v[60:63], v[244:247], v[186:189], v[60:63]
	buffer_load_dwordx4 v[8:11], v160, s[16:19], s75 offen
	s_waitcnt vmcnt(11)
	v_cvt_pk_bf16_f32 v19, v18, v19
	v_cvt_pk_bf16_f32 v18, v16, v17
	v_mfma_f32_16x16x32_bf16 v[56:59], v[248:251], v[186:189], v[56:59]
	ds_write_b64 v161, v[18:19] offset:61184
	v_mfma_f32_16x16x32_bf16 v[52:55], v[202:205], v[186:189], v[52:55]
	buffer_load_dwordx4 v[16:19], v160, s[16:19], s76 offen
	v_mfma_f32_16x16x32_bf16 v[48:51], v[206:209], v[186:189], v[48:51]
	s_waitcnt vmcnt(8)
	s_mov_b32 m0, s56
	s_waitcnt lgkmcnt(0)
	s_barrier
	ds_read_b64_tr_b16 v[170:171], v166 offset:34816
	ds_read_b64_tr_b16 v[172:173], v167 offset:34816
	ds_read_b64_tr_b16 v[176:177], v167 offset:34848
	ds_read_b128 v[178:181], v162 offset:32768
	ds_read_b64_tr_b16 v[174:175], v166 offset:34848
	ds_read_b64_tr_b16 v[182:183], v166 offset:34880
	ds_read_b64_tr_b16 v[186:187], v166 offset:34912
	ds_read_b64_tr_b16 v[184:185], v167 offset:34880
	ds_read_b64_tr_b16 v[188:189], v167 offset:34912
	ds_read_b128 v[190:193], v162 offset:34816
	ds_read_b128 v[198:201], v162 offset:36864
	buffer_load_dwordx4 v163, s[20:23], s45 offen lds
	s_mov_b32 m0, s57
	v_mfma_f32_16x16x32_bf16 v[44:47], v[244:247], v[252:255], v[44:47]
	v_mfma_f32_16x16x32_bf16 v[40:43], v[248:251], v[252:255], v[40:43]
	v_mfma_f32_16x16x32_bf16 v[36:39], v[202:205], v[252:255], v[36:39]
	v_mfma_f32_16x16x32_bf16 v[32:35], v[206:209], v[252:255], v[32:35]
	s_waitcnt lgkmcnt(7)
	v_mfma_f32_16x16x32_bf16 v[156:159], v[170:173], v[178:181], v[156:159]
	buffer_load_dwordx4 v165, s[20:23], s45 offen lds
	s_add_i32 s69, s13, 0xfffa0000
	s_waitcnt lgkmcnt(6)
	v_mfma_f32_16x16x32_bf16 v[152:155], v[174:177], v[178:181], v[152:155]
	s_waitcnt lgkmcnt(3)
	v_mfma_f32_16x16x32_bf16 v[148:151], v[182:185], v[178:181], v[148:151]
	s_waitcnt lgkmcnt(2)
	v_mfma_f32_16x16x32_bf16 v[144:147], v[186:189], v[178:181], v[144:147]
	s_waitcnt lgkmcnt(1)
	v_mfma_f32_16x16x32_bf16 v[140:143], v[170:173], v[190:193], v[140:143]
	s_mov_b32 m0, s58
	s_nop 0
	buffer_load_dwordx4 v164, s[20:23], s45 offen lds
	ds_read_b128 v[178:181], v162 offset:38912
	s_waitcnt vmcnt(10)
	v_cvt_pk_bf16_f32 v15, v14, v15
	v_cvt_pk_bf16_f32 v14, v12, v13
	v_mfma_f32_16x16x32_bf16 v[136:139], v[174:177], v[190:193], v[136:139]
	ds_write_b64 v161, v[14:15]
	v_mfma_f32_16x16x32_bf16 v[132:135], v[182:185], v[190:193], v[132:135]
	s_mov_b32 m0, s59
	s_nop 0
	buffer_load_dwordx4 v168, s[20:23], s45 offen lds
	v_mfma_f32_16x16x32_bf16 v[128:131], v[186:189], v[190:193], v[128:131]
	s_waitcnt lgkmcnt(2)
	v_mfma_f32_16x16x32_bf16 v[124:127], v[170:173], v[198:201], v[124:127]
	ds_read_b128 v[190:193], v162 offset:40960
	v_mfma_f32_16x16x32_bf16 v[120:123], v[174:177], v[198:201], v[120:123]
	v_mfma_f32_16x16x32_bf16 v[116:119], v[182:185], v[198:201], v[116:119]
	v_mfma_f32_16x16x32_bf16 v[112:115], v[186:189], v[198:201], v[112:115]
	s_waitcnt lgkmcnt(2)
	v_mfma_f32_16x16x32_bf16 v[108:111], v[170:173], v[178:181], v[108:111]
	ds_read_b128 v[198:201], v162 offset:43008
	buffer_load_dwordx4 v[12:15], v160, s[24:27], s69 offen
	s_waitcnt vmcnt(11)
	v_cvt_pk_bf16_f32 v3, v2, v3
	v_cvt_pk_bf16_f32 v2, v0, v1
	v_mfma_f32_16x16x32_bf16 v[104:107], v[174:177], v[178:181], v[104:107]
	ds_write_b64 v161, v[2:3] offset:8704
	v_mfma_f32_16x16x32_bf16 v[100:103], v[182:185], v[178:181], v[100:103]
	v_mfma_f32_16x16x32_bf16 v[96:99], v[186:189], v[178:181], v[96:99]
	s_add_i32 s74, s13, 0xfffc0000
	s_waitcnt lgkmcnt(2)
; #define G_DMA_A(kt, AO) do { G_DMA1(kt, AO, 0); G_DMA1(kt, AO, 1); G_DMA1(kt, AO, 2); G_DMA1(kt, AO, 3); if (MF == 9) G_DMA5(kt, AO); } while (0)
; #define G_ISSUE_B(kt) do { const unsigned _sb = (unsigned)(kt) * 4u * kstepB; \
;         _Pragma("unroll") for (int _i = 0; _i < 8; ++_i) sb[_i] = bload16(_i < 4 ? rsB0 : rsB1, vob, _sb + (_i & 3) * kstepB); } while (0)
; #define G_WRITE_B(BO) do { \
;         _Pragma("unroll") for (int _i = 0; _i < 8; ++_i) *(LAS u32x2*)(b_wr + (BO) + (_i & 3) * (16 * G_BSTRIDE) + (_i >> 2) * SLAB1) = pack4(__builtin_bit_cast(f32x4, sb[_i])); } while (0)
; #define G_ENDTILE(VM) do { asm volatile("s_waitcnt vmcnt(" #VM ")" ::: "memory"); \
;         asm volatile("s_waitcnt lgkmcnt(0)" ::: "memory"); __builtin_amdgcn_s_barrier(); asm volatile("" ::: "memory"); } while (0)
;     ...
;     __builtin_amdgcn_s_barrier();
;     G_DMA_A(0, G_A0); G_ISSUE_B(0); G_WRITE_B(G_B0);
;     __builtin_amdgcn_sched_barrier(0);
;     G_ISSUE_B(1);
;     __builtin_amdgcn_sched_barrier(0);
;     G_ENDTILE(8);
;     for (int ui = 0;; ++ui) {
; #pragma unroll
;         for (int m = 0; m < MF; ++m)
; #pragma unroll
;             for (int n = 0; n < 4; ++n) acc[m][n] = (f32x4){0.f, 0.f, 0.f, 0.f};
;         for (int t = 0; t < nt - 2; t += 2) {
;             G_TILE(G_A0, G_B0, true, G_B1, G_A1, t + 1, true, t + 2, (void)0);
;             G_ENDTILE(8);
;             G_TILE(G_A1, G_B1, true, G_B0, G_A0, t + 2, true, t + 3, (void)0);
;             G_ENDTILE(8);
;         }
	v_mfma_f32_16x16x32_bf16 v[92:95], v[170:173], v[190:193], v[92:95]
	ds_read_b128 v[178:181], v162 offset:45056
	v_mfma_f32_16x16x32_bf16 v[88:91], v[174:177], v[190:193], v[88:91]
	v_mfma_f32_16x16x32_bf16 v[84:87], v[182:185], v[190:193], v[84:87]
	v_mfma_f32_16x16x32_bf16 v[80:83], v[186:189], v[190:193], v[80:83]
	s_waitcnt lgkmcnt(2)
	v_mfma_f32_16x16x32_bf16 v[76:79], v[170:173], v[198:201], v[76:79]
	ds_read_b128 v[190:193], v162 offset:47104
	buffer_load_dwordx4 v[0:3], v160, s[24:27], s74 offen
	s_waitcnt vmcnt(11)
	v_cvt_pk_bf16_f32 v31, v30, v31
	v_cvt_pk_bf16_f32 v30, v28, v29
	v_mfma_f32_16x16x32_bf16 v[72:75], v[174:177], v[198:201], v[72:75]
	ds_write_b64 v161, v[30:31] offset:17408
	v_mfma_f32_16x16x32_bf16 v[68:71], v[182:185], v[198:201], v[68:71]
	v_mfma_f32_16x16x32_bf16 v[64:67], v[186:189], v[198:201], v[64:67]
	s_add_i32 s75, s13, 0xfffe0000
	s_waitcnt lgkmcnt(2)
	v_mfma_f32_16x16x32_bf16 v[60:63], v[170:173], v[178:181], v[60:63]
	ds_read_b128 v[198:201], v162 offset:33792
	v_mfma_f32_16x16x32_bf16 v[56:59], v[174:177], v[178:181], v[56:59]
	v_mfma_f32_16x16x32_bf16 v[52:55], v[182:185], v[178:181], v[52:55]
	v_mfma_f32_16x16x32_bf16 v[48:51], v[186:189], v[178:181], v[48:51]
	s_waitcnt lgkmcnt(2)
	v_mfma_f32_16x16x32_bf16 v[44:47], v[170:173], v[190:193], v[44:47]
	ds_read_b128 v[170:173], v162 offset:35840
	buffer_load_dwordx4 v[28:31], v160, s[24:27], s75 offen
	s_waitcnt vmcnt(11)
	v_cvt_pk_bf16_f32 v27, v26, v27
	v_cvt_pk_bf16_f32 v26, v24, v25
	v_mfma_f32_16x16x32_bf16 v[40:43], v[174:177], v[190:193], v[40:43]
	ds_read_b64_tr_b16 v[244:245], v166 offset:52224
	ds_read_b64_tr_b16 v[248:249], v166 offset:52256
	ds_read_b64_tr_b16 v[202:203], v166 offset:52288
	ds_read_b64_tr_b16 v[206:207], v166 offset:52320
	ds_read_b64_tr_b16 v[246:247], v167 offset:52224
	ds_read_b64_tr_b16 v[250:251], v167 offset:52256
	ds_read_b64_tr_b16 v[204:205], v167 offset:52288
	ds_read_b64_tr_b16 v[208:209], v167 offset:52320
	ds_write_b64 v161, v[26:27] offset:26112
	v_mfma_f32_16x16x32_bf16 v[36:39], v[182:185], v[190:193], v[36:39]
	v_mfma_f32_16x16x32_bf16 v[32:35], v[186:189], v[190:193], v[32:35]
	s_waitcnt lgkmcnt(4)
	v_mfma_f32_16x16x32_bf16 v[156:159], v[244:247], v[198:201], v[156:159]
	ds_read_b128 v[182:185], v162 offset:37888
	s_waitcnt lgkmcnt(4)
	v_mfma_f32_16x16x32_bf16 v[152:155], v[248:251], v[198:201], v[152:155]
	s_waitcnt lgkmcnt(3)
	v_mfma_f32_16x16x32_bf16 v[148:151], v[202:205], v[198:201], v[148:151]
	s_waitcnt lgkmcnt(2)
	v_mfma_f32_16x16x32_bf16 v[144:147], v[206:209], v[198:201], v[144:147]
	v_mfma_f32_16x16x32_bf16 v[140:143], v[244:247], v[170:173], v[140:143]
	ds_read_b128 v[186:189], v162 offset:39936
	buffer_load_dwordx4 v[24:27], v160, s[24:27], s13 offen
	s_waitcnt vmcnt(11)
	v_cvt_pk_bf16_f32 v23, v22, v23
	v_cvt_pk_bf16_f32 v22, v20, v21
	v_mfma_f32_16x16x32_bf16 v[136:139], v[248:251], v[170:173], v[136:139]
	ds_write_b64 v161, v[22:23] offset:256
	v_mfma_f32_16x16x32_bf16 v[132:135], v[202:205], v[170:173], v[132:135]
	v_mfma_f32_16x16x32_bf16 v[128:131], v[206:209], v[170:173], v[128:131]
	s_waitcnt lgkmcnt(2)
	v_mfma_f32_16x16x32_bf16 v[124:127], v[244:247], v[182:185], v[124:127]
	ds_read_b128 v[170:173], v162 offset:41984
	v_mfma_f32_16x16x32_bf16 v[120:123], v[248:251], v[182:185], v[120:123]
	v_mfma_f32_16x16x32_bf16 v[116:119], v[202:205], v[182:185], v[116:119]
	v_mfma_f32_16x16x32_bf16 v[112:115], v[206:209], v[182:185], v[112:115]
	s_waitcnt lgkmcnt(2)
	v_mfma_f32_16x16x32_bf16 v[108:111], v[244:247], v[186:189], v[108:111]
	ds_read_b128 v[182:185], v162 offset:44032
	buffer_load_dwordx4 v[20:23], v160, s[16:19], s69 offen
	s_waitcnt vmcnt(11)
	v_cvt_pk_bf16_f32 v7, v6, v7
	v_cvt_pk_bf16_f32 v6, v4, v5
	v_mfma_f32_16x16x32_bf16 v[104:107], v[248:251], v[186:189], v[104:107]
	ds_write_b64 v161, v[6:7] offset:8960
	v_mfma_f32_16x16x32_bf16 v[100:103], v[202:205], v[186:189], v[100:103]
	v_mfma_f32_16x16x32_bf16 v[96:99], v[206:209], v[186:189], v[96:99]
	s_waitcnt lgkmcnt(2)
	v_mfma_f32_16x16x32_bf16 v[92:95], v[244:247], v[170:173], v[92:95]
	ds_read_b128 v[186:189], v162 offset:46080
	v_mfma_f32_16x16x32_bf16 v[88:91], v[248:251], v[170:173], v[88:91]
	v_mfma_f32_16x16x32_bf16 v[84:87], v[202:205], v[170:173], v[84:87]
	v_mfma_f32_16x16x32_bf16 v[80:83], v[206:209], v[170:173], v[80:83]
	s_waitcnt lgkmcnt(2)
	v_mfma_f32_16x16x32_bf16 v[76:79], v[244:247], v[182:185], v[76:79]
	ds_read_b128 v[252:255], v162 offset:48128
	buffer_load_dwordx4 v[4:7], v160, s[16:19], s74 offen
	s_waitcnt vmcnt(11)
	v_cvt_pk_bf16_f32 v11, v10, v11
	v_cvt_pk_bf16_f32 v10, v8, v9
	v_mfma_f32_16x16x32_bf16 v[72:75], v[248:251], v[182:185], v[72:75]
	ds_write_b64 v161, v[10:11] offset:17664
	v_mfma_f32_16x16x32_bf16 v[68:71], v[202:205], v[182:185], v[68:71]
	v_mfma_f32_16x16x32_bf16 v[64:67], v[206:209], v[182:185], v[64:67]
	s_waitcnt lgkmcnt(2)
	v_mfma_f32_16x16x32_bf16 v[60:63], v[244:247], v[186:189], v[60:63]
	buffer_load_dwordx4 v[8:11], v160, s[16:19], s75 offen
	s_waitcnt vmcnt(11)
	v_cvt_pk_bf16_f32 v19, v18, v19
	v_cvt_pk_bf16_f32 v18, v16, v17
	v_mfma_f32_16x16x32_bf16 v[56:59], v[248:251], v[186:189], v[56:59]
	ds_write_b64 v161, v[18:19] offset:26368
	v_mfma_f32_16x16x32_bf16 v[52:55], v[202:205], v[186:189], v[52:55]
	buffer_load_dwordx4 v[16:19], v160, s[16:19], s13 offen
	v_mfma_f32_16x16x32_bf16 v[48:51], v[206:209], v[186:189], v[48:51]
	s_waitcnt vmcnt(8)
	s_waitcnt lgkmcnt(0)
	s_barrier
	s_add_i32 s12, s12, 2
	s_add_i32 s13, s13, 0x100000
	s_addk_i32 s45, 0x100
	s_cmp_ge_i32 s12, s30
	s_cbranch_scc0 .LBB0_899
	v_mfma_f32_16x16x32_bf16 v[44:47], v[244:247], v[252:255], v[44:47]
	v_mfma_f32_16x16x32_bf16 v[40:43], v[248:251], v[252:255], v[40:43]
	v_mfma_f32_16x16x32_bf16 v[36:39], v[202:205], v[252:255], v[36:39]
	v_mfma_f32_16x16x32_bf16 v[32:35], v[206:209], v[252:255], v[32:35]
	s_branch .LBB0_901

; #define G_DMA_A(kt, AO) do { G_DMA1(kt, AO, 0); G_DMA1(kt, AO, 1); G_DMA1(kt, AO, 2); G_DMA1(kt, AO, 3); if (MF == 9) G_DMA5(kt, AO); } while (0)
; #define G_ISSUE_B(kt) do { const unsigned _sb = (unsigned)(kt) * 4u * kstepB; \
;         _Pragma("unroll") for (int _i = 0; _i < 8; ++_i) sb[_i] = bload16(_i < 4 ? rsB0 : rsB1, vob, _sb + (_i & 3) * kstepB); } while (0)
; #define G_WRITE_B(BO) do { \
;         _Pragma("unroll") for (int _i = 0; _i < 8; ++_i) *(LAS u32x2*)(b_wr + (BO) + (_i & 3) * (16 * G_BSTRIDE) + (_i >> 2) * SLAB1) = pack4(__builtin_bit_cast(f32x4, sb[_i])); } while (0)
; #define G_ENDTILE(VM) do { asm volatile("s_waitcnt vmcnt(" #VM ")" ::: "memory"); \
;         asm volatile("s_waitcnt lgkmcnt(0)" ::: "memory"); __builtin_amdgcn_s_barrier(); asm volatile("" ::: "memory"); } while (0)
;     ...
;     __builtin_amdgcn_s_barrier();
;     G_DMA_A(0, G_A0); G_ISSUE_B(0); G_WRITE_B(G_B0);
;     __builtin_amdgcn_sched_barrier(0);
;     G_ISSUE_B(1);
;     __builtin_amdgcn_sched_barrier(0);
;     G_ENDTILE(8);
;     for (int ui = 0;; ++ui) {
; #pragma unroll
;         for (int m = 0; m < MF; ++m)
; #pragma unroll
;             for (int n = 0; n < 4; ++n) acc[m][n] = (f32x4){0.f, 0.f, 0.f, 0.f};
;         for (int t = 0; t < nt - 2; t += 2) {
;             G_TILE(G_A0, G_B0, true, G_B1, G_A1, t + 1, true, t + 2, (void)0);
.LBB0_1038:
	s_mov_b32 m0, s64
	s_add_i32 s5, s4, 0xffffff80
	ds_read_b64_tr_b16 v[160:161], v178
	ds_read_b64_tr_b16 v[162:163], v179
	ds_read_b64_tr_b16 v[166:167], v179 offset:32
	ds_read_b128 v[168:171], v175
	ds_read_b64_tr_b16 v[164:165], v178 offset:32
	ds_read_b64_tr_b16 v[182:183], v178 offset:64
	ds_read_b64_tr_b16 v[186:187], v178 offset:96
	ds_read_b64_tr_b16 v[184:185], v179 offset:64
	ds_read_b64_tr_b16 v[188:189], v179 offset:96
	ds_read_b128 v[190:193], v175 offset:2048
	ds_read_b128 v[194:197], v175 offset:4096
	buffer_load_dwordx4 v176, s[16:19], s5 offen lds
	s_mov_b32 m0, s63
	v_mfma_f32_16x16x32_bf16 v[44:47], v[244:247], v[252:255], v[44:47]
	v_mfma_f32_16x16x32_bf16 v[40:43], v[248:251], v[252:255], v[40:43]
	v_mfma_f32_16x16x32_bf16 v[36:39], v[198:201], v[252:255], v[36:39]
	v_mfma_f32_16x16x32_bf16 v[32:35], v[202:205], v[252:255], v[32:35]
	s_waitcnt lgkmcnt(7)
	v_mfma_f32_16x16x32_bf16 v[156:159], v[160:163], v[168:171], v[156:159]
	buffer_load_dwordx4 v177, s[16:19], s5 offen lds
	s_waitcnt lgkmcnt(6)
	v_mfma_f32_16x16x32_bf16 v[152:155], v[164:167], v[168:171], v[152:155]
	s_waitcnt lgkmcnt(3)
	v_mfma_f32_16x16x32_bf16 v[148:151], v[182:185], v[168:171], v[148:151]
	s_waitcnt lgkmcnt(2)
	v_mfma_f32_16x16x32_bf16 v[144:147], v[186:189], v[168:171], v[144:147]
	s_waitcnt lgkmcnt(1)
	v_mfma_f32_16x16x32_bf16 v[140:143], v[160:163], v[190:193], v[140:143]
	s_mov_b32 m0, s62
	s_nop 0
	buffer_load_dwordx4 v180, s[16:19], s5 offen lds
	ds_read_b128 v[168:171], v175 offset:6144
	s_waitcnt vmcnt(10)
	v_cvt_pk_bf16_f32 v15, v14, v15
	v_cvt_pk_bf16_f32 v14, v12, v13
	v_mfma_f32_16x16x32_bf16 v[136:139], v[164:167], v[190:193], v[136:139]
	ds_write_b64 v174, v[14:15] offset:34816
	v_mfma_f32_16x16x32_bf16 v[132:135], v[182:185], v[190:193], v[132:135]
	s_mov_b32 m0, s61
	s_nop 0
	buffer_load_dwordx4 v181, s[16:19], s5 offen lds
	s_add_i32 s5, s1, 0xfff20000
	v_mfma_f32_16x16x32_bf16 v[128:131], v[186:189], v[190:193], v[128:131]
	s_waitcnt lgkmcnt(2)
	v_mfma_f32_16x16x32_bf16 v[124:127], v[160:163], v[194:197], v[124:127]
	ds_read_b128 v[190:193], v175 offset:8192
	v_mfma_f32_16x16x32_bf16 v[120:123], v[164:167], v[194:197], v[120:123]
	v_mfma_f32_16x16x32_bf16 v[116:119], v[182:185], v[194:197], v[116:119]
	v_mfma_f32_16x16x32_bf16 v[112:115], v[186:189], v[194:197], v[112:115]
	s_waitcnt lgkmcnt(2)
	v_mfma_f32_16x16x32_bf16 v[108:111], v[160:163], v[168:171], v[108:111]
	ds_read_b128 v[194:197], v175 offset:10240
	buffer_load_dwordx4 v[12:15], v173, s[8:11], s5 offen
	s_waitcnt vmcnt(10)
	v_cvt_pk_bf16_f32 v31, v30, v31
	v_cvt_pk_bf16_f32 v30, v28, v29
	v_mfma_f32_16x16x32_bf16 v[104:107], v[164:167], v[168:171], v[104:107]
	ds_write_b64 v174, v[30:31] offset:43520
	v_mfma_f32_16x16x32_bf16 v[100:103], v[182:185], v[168:171], v[100:103]
	v_mfma_f32_16x16x32_bf16 v[96:99], v[186:189], v[168:171], v[96:99]
	s_add_i32 s20, s1, 0xfff40000
	s_waitcnt lgkmcnt(2)
	v_mfma_f32_16x16x32_bf16 v[92:95], v[160:163], v[190:193], v[92:95]
	ds_read_b128 v[168:171], v175 offset:12288
	v_mfma_f32_16x16x32_bf16 v[88:91], v[164:167], v[190:193], v[88:91]
	v_mfma_f32_16x16x32_bf16 v[84:87], v[182:185], v[190:193], v[84:87]
	v_mfma_f32_16x16x32_bf16 v[80:83], v[186:189], v[190:193], v[80:83]
	s_waitcnt lgkmcnt(2)
	v_mfma_f32_16x16x32_bf16 v[76:79], v[160:163], v[194:197], v[76:79]
	ds_read_b128 v[190:193], v175 offset:14336
	v_cvt_pk_bf16_f32 v7, v6, v7
	v_cvt_pk_bf16_f32 v6, v4, v5
	v_mfma_f32_16x16x32_bf16 v[72:75], v[164:167], v[194:197], v[72:75]
	ds_write_b64 v174, v[6:7] offset:52224
	v_mfma_f32_16x16x32_bf16 v[68:71], v[182:185], v[194:197], v[68:71]
	v_mfma_f32_16x16x32_bf16 v[64:67], v[186:189], v[194:197], v[64:67]
	s_add_i32 s21, s1, 0xfff60000
	buffer_load_dwordx4 v[28:31], v173, s[8:11], s20 offen
	s_waitcnt lgkmcnt(2)
	v_mfma_f32_16x16x32_bf16 v[60:63], v[160:163], v[168:171], v[60:63]
	ds_read_b128 v[194:197], v175 offset:1024
	v_mfma_f32_16x16x32_bf16 v[56:59], v[164:167], v[168:171], v[56:59]
	v_mfma_f32_16x16x32_bf16 v[52:55], v[182:185], v[168:171], v[52:55]
	v_mfma_f32_16x16x32_bf16 v[48:51], v[186:189], v[168:171], v[48:51]
	s_waitcnt lgkmcnt(2)
	v_mfma_f32_16x16x32_bf16 v[44:47], v[160:163], v[190:193], v[44:47]
	ds_read_b128 v[160:163], v175 offset:3072
	buffer_load_dwordx4 v[4:7], v173, s[8:11], s21 offen
	s_waitcnt vmcnt(11)
	v_cvt_pk_bf16_f32 v27, v26, v27
	v_cvt_pk_bf16_f32 v26, v24, v25
	v_mfma_f32_16x16x32_bf16 v[40:43], v[164:167], v[190:193], v[40:43]
	ds_read_b64_tr_b16 v[244:245], v178 offset:17408
	ds_read_b64_tr_b16 v[248:249], v178 offset:17440
	ds_read_b64_tr_b16 v[198:199], v178 offset:17472
	ds_read_b64_tr_b16 v[202:203], v178 offset:17504
	ds_read_b64_tr_b16 v[246:247], v179 offset:17408
	ds_read_b64_tr_b16 v[250:251], v179 offset:17440
	ds_read_b64_tr_b16 v[200:201], v179 offset:17472
	ds_read_b64_tr_b16 v[204:205], v179 offset:17504
	ds_write_b64 v174, v[26:27] offset:60928
	v_mfma_f32_16x16x32_bf16 v[36:39], v[182:185], v[190:193], v[36:39]
	v_mfma_f32_16x16x32_bf16 v[32:35], v[186:189], v[190:193], v[32:35]
	s_add_i32 s22, s1, 0xfff80000
	s_waitcnt lgkmcnt(4)
	v_mfma_f32_16x16x32_bf16 v[156:159], v[244:247], v[194:197], v[156:159]
	ds_read_b128 v[182:185], v175 offset:5120
	s_waitcnt lgkmcnt(4)
	v_mfma_f32_16x16x32_bf16 v[152:155], v[248:251], v[194:197], v[152:155]
	s_waitcnt lgkmcnt(3)
	v_mfma_f32_16x16x32_bf16 v[148:151], v[198:201], v[194:197], v[148:151]
	s_waitcnt lgkmcnt(2)
	v_mfma_f32_16x16x32_bf16 v[144:147], v[202:205], v[194:197], v[144:147]
	v_mfma_f32_16x16x32_bf16 v[140:143], v[244:247], v[160:163], v[140:143]
	ds_read_b128 v[186:189], v175 offset:7168
	buffer_load_dwordx4 v[24:27], v173, s[8:11], s22 offen
	s_waitcnt vmcnt(11)
; #define G_DMA_A(kt, AO) do { G_DMA1(kt, AO, 0); G_DMA1(kt, AO, 1); G_DMA1(kt, AO, 2); G_DMA1(kt, AO, 3); if (MF == 9) G_DMA5(kt, AO); } while (0)
; #define G_ISSUE_B(kt) do { const unsigned _sb = (unsigned)(kt) * 4u * kstepB; \
;         _Pragma("unroll") for (int _i = 0; _i < 8; ++_i) sb[_i] = bload16(_i < 4 ? rsB0 : rsB1, vob, _sb + (_i & 3) * kstepB); } while (0)
; #define G_WRITE_B(BO) do { \
;         _Pragma("unroll") for (int _i = 0; _i < 8; ++_i) *(LAS u32x2*)(b_wr + (BO) + (_i & 3) * (16 * G_BSTRIDE) + (_i >> 2) * SLAB1) = pack4(__builtin_bit_cast(f32x4, sb[_i])); } while (0)
; #define G_ENDTILE(VM) do { asm volatile("s_waitcnt vmcnt(" #VM ")" ::: "memory"); \
;         asm volatile("s_waitcnt lgkmcnt(0)" ::: "memory"); __builtin_amdgcn_s_barrier(); asm volatile("" ::: "memory"); } while (0)
;     ...
;     __builtin_amdgcn_s_barrier();
;     G_DMA_A(0, G_A0); G_ISSUE_B(0); G_WRITE_B(G_B0);
;     __builtin_amdgcn_sched_barrier(0);
;     G_ISSUE_B(1);
;     __builtin_amdgcn_sched_barrier(0);
;     G_ENDTILE(8);
;     for (int ui = 0;; ++ui) {
; #pragma unroll
;         for (int m = 0; m < MF; ++m)
; #pragma unroll
;             for (int n = 0; n < 4; ++n) acc[m][n] = (f32x4){0.f, 0.f, 0.f, 0.f};
;         for (int t = 0; t < nt - 2; t += 2) {
;             G_TILE(G_A0, G_B0, true, G_B1, G_A1, t + 1, true, t + 2, (void)0);
;             G_ENDTILE(8);
;             G_TILE(G_A1, G_B1, true, G_B0, G_A0, t + 2, true, t + 3, (void)0);
;             G_ENDTILE(8);
	v_cvt_pk_bf16_f32 v23, v22, v23
	v_cvt_pk_bf16_f32 v22, v20, v21
	v_mfma_f32_16x16x32_bf16 v[136:139], v[248:251], v[160:163], v[136:139]
	ds_write_b64 v174, v[22:23] offset:35072
	v_mfma_f32_16x16x32_bf16 v[132:135], v[198:201], v[160:163], v[132:135]
	v_mfma_f32_16x16x32_bf16 v[128:131], v[202:205], v[160:163], v[128:131]
	s_waitcnt lgkmcnt(2)
	v_mfma_f32_16x16x32_bf16 v[124:127], v[244:247], v[182:185], v[124:127]
	ds_read_b128 v[160:163], v175 offset:9216
	v_mfma_f32_16x16x32_bf16 v[120:123], v[248:251], v[182:185], v[120:123]
	v_mfma_f32_16x16x32_bf16 v[116:119], v[198:201], v[182:185], v[116:119]
	v_mfma_f32_16x16x32_bf16 v[112:115], v[202:205], v[182:185], v[112:115]
	s_waitcnt lgkmcnt(2)
	v_mfma_f32_16x16x32_bf16 v[108:111], v[244:247], v[186:189], v[108:111]
	ds_read_b128 v[182:185], v175 offset:11264
	buffer_load_dwordx4 v[20:23], v173, s[12:15], s5 offen
	s_waitcnt vmcnt(10)
	v_cvt_pk_bf16_f32 v11, v10, v11
	v_cvt_pk_bf16_f32 v10, v8, v9
	v_mfma_f32_16x16x32_bf16 v[104:107], v[248:251], v[186:189], v[104:107]
	ds_write_b64 v174, v[10:11] offset:43776
	v_mfma_f32_16x16x32_bf16 v[100:103], v[198:201], v[186:189], v[100:103]
	v_mfma_f32_16x16x32_bf16 v[96:99], v[202:205], v[186:189], v[96:99]
	s_waitcnt lgkmcnt(2)
	v_mfma_f32_16x16x32_bf16 v[92:95], v[244:247], v[160:163], v[92:95]
	ds_read_b128 v[186:189], v175 offset:13312
	v_mfma_f32_16x16x32_bf16 v[88:91], v[248:251], v[160:163], v[88:91]
	v_mfma_f32_16x16x32_bf16 v[84:87], v[198:201], v[160:163], v[84:87]
	v_mfma_f32_16x16x32_bf16 v[80:83], v[202:205], v[160:163], v[80:83]
	s_waitcnt lgkmcnt(2)
	v_mfma_f32_16x16x32_bf16 v[76:79], v[244:247], v[182:185], v[76:79]
	ds_read_b128 v[252:255], v175 offset:15360
	v_cvt_pk_bf16_f32 v3, v2, v3
	v_cvt_pk_bf16_f32 v2, v0, v1
	v_mfma_f32_16x16x32_bf16 v[72:75], v[248:251], v[182:185], v[72:75]
	ds_write_b64 v174, v[2:3] offset:52480
	v_mfma_f32_16x16x32_bf16 v[68:71], v[198:201], v[182:185], v[68:71]
	v_mfma_f32_16x16x32_bf16 v[64:67], v[202:205], v[182:185], v[64:67]
	buffer_load_dwordx4 v[8:11], v173, s[12:15], s20 offen
	s_waitcnt lgkmcnt(2)
	v_mfma_f32_16x16x32_bf16 v[60:63], v[244:247], v[186:189], v[60:63]
	buffer_load_dwordx4 v[0:3], v173, s[12:15], s21 offen
	s_waitcnt vmcnt(11)
	v_cvt_pk_bf16_f32 v19, v18, v19
	v_cvt_pk_bf16_f32 v18, v16, v17
	v_mfma_f32_16x16x32_bf16 v[56:59], v[248:251], v[186:189], v[56:59]
	ds_write_b64 v174, v[18:19] offset:61184
	v_mfma_f32_16x16x32_bf16 v[52:55], v[198:201], v[186:189], v[52:55]
	buffer_load_dwordx4 v[16:19], v173, s[12:15], s22 offen
	v_mfma_f32_16x16x32_bf16 v[48:51], v[202:205], v[186:189], v[48:51]
	s_waitcnt vmcnt(8)
	s_mov_b32 m0, s45
	s_waitcnt lgkmcnt(0)
	s_barrier
	ds_read_b64_tr_b16 v[160:161], v178 offset:34816
	ds_read_b64_tr_b16 v[162:163], v179 offset:34816
	ds_read_b64_tr_b16 v[166:167], v179 offset:34848
	ds_read_b128 v[168:171], v175 offset:32768
	ds_read_b64_tr_b16 v[164:165], v178 offset:34848
	ds_read_b64_tr_b16 v[182:183], v178 offset:34880
	ds_read_b64_tr_b16 v[186:187], v178 offset:34912
	ds_read_b64_tr_b16 v[184:185], v179 offset:34880
	ds_read_b64_tr_b16 v[188:189], v179 offset:34912
	ds_read_b128 v[190:193], v175 offset:34816
	ds_read_b128 v[194:197], v175 offset:36864
	buffer_load_dwordx4 v176, s[16:19], s4 offen lds
	s_mov_b32 m0, s53
	v_mfma_f32_16x16x32_bf16 v[44:47], v[244:247], v[252:255], v[44:47]
	v_mfma_f32_16x16x32_bf16 v[40:43], v[248:251], v[252:255], v[40:43]
	v_mfma_f32_16x16x32_bf16 v[36:39], v[198:201], v[252:255], v[36:39]
	v_mfma_f32_16x16x32_bf16 v[32:35], v[202:205], v[252:255], v[32:35]
	s_waitcnt lgkmcnt(7)
	v_mfma_f32_16x16x32_bf16 v[156:159], v[160:163], v[168:171], v[156:159]
	buffer_load_dwordx4 v177, s[16:19], s4 offen lds
	s_add_i32 s5, s1, 0xfffa0000
	s_waitcnt lgkmcnt(6)
	v_mfma_f32_16x16x32_bf16 v[152:155], v[164:167], v[168:171], v[152:155]
	s_waitcnt lgkmcnt(3)
	v_mfma_f32_16x16x32_bf16 v[148:151], v[182:185], v[168:171], v[148:151]
	s_waitcnt lgkmcnt(2)
	v_mfma_f32_16x16x32_bf16 v[144:147], v[186:189], v[168:171], v[144:147]
	s_waitcnt lgkmcnt(1)
	v_mfma_f32_16x16x32_bf16 v[140:143], v[160:163], v[190:193], v[140:143]
	s_mov_b32 m0, s54
	s_nop 0
	buffer_load_dwordx4 v180, s[16:19], s4 offen lds
	ds_read_b128 v[168:171], v175 offset:38912
	s_waitcnt vmcnt(10)
	v_cvt_pk_bf16_f32 v15, v14, v15
	v_cvt_pk_bf16_f32 v14, v12, v13
	v_mfma_f32_16x16x32_bf16 v[136:139], v[164:167], v[190:193], v[136:139]
	ds_write_b64 v174, v[14:15]
	v_mfma_f32_16x16x32_bf16 v[132:135], v[182:185], v[190:193], v[132:135]
	s_mov_b32 m0, s55
	s_nop 0
	buffer_load_dwordx4 v181, s[16:19], s4 offen lds
	v_mfma_f32_16x16x32_bf16 v[128:131], v[186:189], v[190:193], v[128:131]
	s_waitcnt lgkmcnt(2)
	v_mfma_f32_16x16x32_bf16 v[124:127], v[160:163], v[194:197], v[124:127]
	ds_read_b128 v[190:193], v175 offset:40960
	v_mfma_f32_16x16x32_bf16 v[120:123], v[164:167], v[194:197], v[120:123]
	v_mfma_f32_16x16x32_bf16 v[116:119], v[182:185], v[194:197], v[116:119]
	v_mfma_f32_16x16x32_bf16 v[112:115], v[186:189], v[194:197], v[112:115]
	s_waitcnt lgkmcnt(2)
	v_mfma_f32_16x16x32_bf16 v[108:111], v[160:163], v[168:171], v[108:111]
	ds_read_b128 v[194:197], v175 offset:43008
	buffer_load_dwordx4 v[12:15], v173, s[8:11], s5 offen
	s_waitcnt vmcnt(11)
	v_cvt_pk_bf16_f32 v31, v30, v31
	v_cvt_pk_bf16_f32 v30, v28, v29
	v_mfma_f32_16x16x32_bf16 v[104:107], v[164:167], v[168:171], v[104:107]
	ds_write_b64 v174, v[30:31] offset:8704
	v_mfma_f32_16x16x32_bf16 v[100:103], v[182:185], v[168:171], v[100:103]
	v_mfma_f32_16x16x32_bf16 v[96:99], v[186:189], v[168:171], v[96:99]
	s_add_i32 s20, s1, 0xfffc0000
	s_waitcnt lgkmcnt(2)
; #define G_DMA_A(kt, AO) do { G_DMA1(kt, AO, 0); G_DMA1(kt, AO, 1); G_DMA1(kt, AO, 2); G_DMA1(kt, AO, 3); if (MF == 9) G_DMA5(kt, AO); } while (0)
; #define G_ISSUE_B(kt) do { const unsigned _sb = (unsigned)(kt) * 4u * kstepB; \
;         _Pragma("unroll") for (int _i = 0; _i < 8; ++_i) sb[_i] = bload16(_i < 4 ? rsB0 : rsB1, vob, _sb + (_i & 3) * kstepB); } while (0)
; #define G_WRITE_B(BO) do { \
;         _Pragma("unroll") for (int _i = 0; _i < 8; ++_i) *(LAS u32x2*)(b_wr + (BO) + (_i & 3) * (16 * G_BSTRIDE) + (_i >> 2) * SLAB1) = pack4(__builtin_bit_cast(f32x4, sb[_i])); } while (0)
; #define G_ENDTILE(VM) do { asm volatile("s_waitcnt vmcnt(" #VM ")" ::: "memory"); \
;         asm volatile("s_waitcnt lgkmcnt(0)" ::: "memory"); __builtin_amdgcn_s_barrier(); asm volatile("" ::: "memory"); } while (0)
;     ...
;     __builtin_amdgcn_s_barrier();
;     G_DMA_A(0, G_A0); G_ISSUE_B(0); G_WRITE_B(G_B0);
;     __builtin_amdgcn_sched_barrier(0);
;     G_ISSUE_B(1);
;     __builtin_amdgcn_sched_barrier(0);
;     G_ENDTILE(8);
;     for (int ui = 0;; ++ui) {
; #pragma unroll
;         for (int m = 0; m < MF; ++m)
; #pragma unroll
;             for (int n = 0; n < 4; ++n) acc[m][n] = (f32x4){0.f, 0.f, 0.f, 0.f};
;         for (int t = 0; t < nt - 2; t += 2) {
;             G_TILE(G_A0, G_B0, true, G_B1, G_A1, t + 1, true, t + 2, (void)0);
;             G_ENDTILE(8);
;             G_TILE(G_A1, G_B1, true, G_B0, G_A0, t + 2, true, t + 3, (void)0);
;             G_ENDTILE(8);
;         }
	v_mfma_f32_16x16x32_bf16 v[92:95], v[160:163], v[190:193], v[92:95]
	ds_read_b128 v[168:171], v175 offset:45056
	v_mfma_f32_16x16x32_bf16 v[88:91], v[164:167], v[190:193], v[88:91]
	v_mfma_f32_16x16x32_bf16 v[84:87], v[182:185], v[190:193], v[84:87]
	v_mfma_f32_16x16x32_bf16 v[80:83], v[186:189], v[190:193], v[80:83]
	s_waitcnt lgkmcnt(2)
	v_mfma_f32_16x16x32_bf16 v[76:79], v[160:163], v[194:197], v[76:79]
	ds_read_b128 v[190:193], v175 offset:47104
	buffer_load_dwordx4 v[28:31], v173, s[8:11], s20 offen
	s_waitcnt vmcnt(11)
	v_cvt_pk_bf16_f32 v7, v6, v7
	v_cvt_pk_bf16_f32 v6, v4, v5
	v_mfma_f32_16x16x32_bf16 v[72:75], v[164:167], v[194:197], v[72:75]
	ds_write_b64 v174, v[6:7] offset:17408
	v_mfma_f32_16x16x32_bf16 v[68:71], v[182:185], v[194:197], v[68:71]
	v_mfma_f32_16x16x32_bf16 v[64:67], v[186:189], v[194:197], v[64:67]
	s_add_i32 s21, s1, 0xfffe0000
	s_waitcnt lgkmcnt(2)
	v_mfma_f32_16x16x32_bf16 v[60:63], v[160:163], v[168:171], v[60:63]
	ds_read_b128 v[194:197], v175 offset:33792
	v_mfma_f32_16x16x32_bf16 v[56:59], v[164:167], v[168:171], v[56:59]
	v_mfma_f32_16x16x32_bf16 v[52:55], v[182:185], v[168:171], v[52:55]
	v_mfma_f32_16x16x32_bf16 v[48:51], v[186:189], v[168:171], v[48:51]
	s_waitcnt lgkmcnt(2)
	v_mfma_f32_16x16x32_bf16 v[44:47], v[160:163], v[190:193], v[44:47]
	ds_read_b128 v[160:163], v175 offset:35840
	buffer_load_dwordx4 v[4:7], v173, s[8:11], s21 offen
	s_waitcnt vmcnt(11)
	v_cvt_pk_bf16_f32 v27, v26, v27
	v_cvt_pk_bf16_f32 v26, v24, v25
	v_mfma_f32_16x16x32_bf16 v[40:43], v[164:167], v[190:193], v[40:43]
	ds_read_b64_tr_b16 v[244:245], v178 offset:52224
	ds_read_b64_tr_b16 v[248:249], v178 offset:52256
	ds_read_b64_tr_b16 v[198:199], v178 offset:52288
	ds_read_b64_tr_b16 v[202:203], v178 offset:52320
	ds_read_b64_tr_b16 v[246:247], v179 offset:52224
	ds_read_b64_tr_b16 v[250:251], v179 offset:52256
	ds_read_b64_tr_b16 v[200:201], v179 offset:52288
	ds_read_b64_tr_b16 v[204:205], v179 offset:52320
	ds_write_b64 v174, v[26:27] offset:26112
	v_mfma_f32_16x16x32_bf16 v[36:39], v[182:185], v[190:193], v[36:39]
	v_mfma_f32_16x16x32_bf16 v[32:35], v[186:189], v[190:193], v[32:35]
	s_waitcnt lgkmcnt(4)
	v_mfma_f32_16x16x32_bf16 v[156:159], v[244:247], v[194:197], v[156:159]
	ds_read_b128 v[182:185], v175 offset:37888
	s_waitcnt lgkmcnt(4)
	v_mfma_f32_16x16x32_bf16 v[152:155], v[248:251], v[194:197], v[152:155]
	s_waitcnt lgkmcnt(3)
	v_mfma_f32_16x16x32_bf16 v[148:151], v[198:201], v[194:197], v[148:151]
	s_waitcnt lgkmcnt(2)
	v_mfma_f32_16x16x32_bf16 v[144:147], v[202:205], v[194:197], v[144:147]
	v_mfma_f32_16x16x32_bf16 v[140:143], v[244:247], v[160:163], v[140:143]
	ds_read_b128 v[186:189], v175 offset:39936
	buffer_load_dwordx4 v[24:27], v173, s[8:11], s1 offen
	s_waitcnt vmcnt(11)
	v_cvt_pk_bf16_f32 v23, v22, v23
	v_cvt_pk_bf16_f32 v22, v20, v21
	v_mfma_f32_16x16x32_bf16 v[136:139], v[248:251], v[160:163], v[136:139]
	ds_write_b64 v174, v[22:23] offset:256
	v_mfma_f32_16x16x32_bf16 v[132:135], v[198:201], v[160:163], v[132:135]
	v_mfma_f32_16x16x32_bf16 v[128:131], v[202:205], v[160:163], v[128:131]
	s_waitcnt lgkmcnt(2)
	v_mfma_f32_16x16x32_bf16 v[124:127], v[244:247], v[182:185], v[124:127]
	ds_read_b128 v[160:163], v175 offset:41984
	v_mfma_f32_16x16x32_bf16 v[120:123], v[248:251], v[182:185], v[120:123]
	v_mfma_f32_16x16x32_bf16 v[116:119], v[198:201], v[182:185], v[116:119]
	v_mfma_f32_16x16x32_bf16 v[112:115], v[202:205], v[182:185], v[112:115]
	s_waitcnt lgkmcnt(2)
	v_mfma_f32_16x16x32_bf16 v[108:111], v[244:247], v[186:189], v[108:111]
	ds_read_b128 v[182:185], v175 offset:44032
	buffer_load_dwordx4 v[20:23], v173, s[12:15], s5 offen
	s_waitcnt vmcnt(11)
	v_cvt_pk_bf16_f32 v11, v10, v11
	v_cvt_pk_bf16_f32 v10, v8, v9
	v_mfma_f32_16x16x32_bf16 v[104:107], v[248:251], v[186:189], v[104:107]
	ds_write_b64 v174, v[10:11] offset:8960
	v_mfma_f32_16x16x32_bf16 v[100:103], v[198:201], v[186:189], v[100:103]
	v_mfma_f32_16x16x32_bf16 v[96:99], v[202:205], v[186:189], v[96:99]
	s_waitcnt lgkmcnt(2)
	v_mfma_f32_16x16x32_bf16 v[92:95], v[244:247], v[160:163], v[92:95]
	ds_read_b128 v[186:189], v175 offset:46080
	v_mfma_f32_16x16x32_bf16 v[88:91], v[248:251], v[160:163], v[88:91]
	v_mfma_f32_16x16x32_bf16 v[84:87], v[198:201], v[160:163], v[84:87]
	v_mfma_f32_16x16x32_bf16 v[80:83], v[202:205], v[160:163], v[80:83]
	s_waitcnt lgkmcnt(2)
	v_mfma_f32_16x16x32_bf16 v[76:79], v[244:247], v[182:185], v[76:79]
	ds_read_b128 v[252:255], v175 offset:48128
	buffer_load_dwordx4 v[8:11], v173, s[12:15], s20 offen
	s_waitcnt vmcnt(11)
	v_cvt_pk_bf16_f32 v3, v2, v3
	v_cvt_pk_bf16_f32 v2, v0, v1
	v_mfma_f32_16x16x32_bf16 v[72:75], v[248:251], v[182:185], v[72:75]
	ds_write_b64 v174, v[2:3] offset:17664
	v_mfma_f32_16x16x32_bf16 v[68:71], v[198:201], v[182:185], v[68:71]
	v_mfma_f32_16x16x32_bf16 v[64:67], v[202:205], v[182:185], v[64:67]
	s_waitcnt lgkmcnt(2)
	v_mfma_f32_16x16x32_bf16 v[60:63], v[244:247], v[186:189], v[60:63]
	buffer_load_dwordx4 v[0:3], v173, s[12:15], s21 offen
	s_waitcnt vmcnt(11)
	v_cvt_pk_bf16_f32 v19, v18, v19
	v_cvt_pk_bf16_f32 v18, v16, v17
	v_mfma_f32_16x16x32_bf16 v[56:59], v[248:251], v[186:189], v[56:59]
	ds_write_b64 v174, v[18:19] offset:26368
	v_mfma_f32_16x16x32_bf16 v[52:55], v[198:201], v[186:189], v[52:55]
	buffer_load_dwordx4 v[16:19], v173, s[12:15], s1 offen
	v_mfma_f32_16x16x32_bf16 v[48:51], v[202:205], v[186:189], v[48:51]
	s_waitcnt vmcnt(8)
	s_waitcnt lgkmcnt(0)
	s_barrier
	s_add_i32 s0, s0, 2
	s_add_i32 s1, s1, 0x100000
	s_addk_i32 s4, 0x100
	s_cmp_ge_i32 s0, s60
	s_cbranch_scc0 .LBB0_1038
	v_mfma_f32_16x16x32_bf16 v[44:47], v[244:247], v[252:255], v[44:47]
	v_mfma_f32_16x16x32_bf16 v[40:43], v[248:251], v[252:255], v[40:43]
	v_mfma_f32_16x16x32_bf16 v[36:39], v[198:201], v[252:255], v[36:39]
	v_mfma_f32_16x16x32_bf16 v[32:35], v[202:205], v[252:255], v[32:35]
	s_branch .LBB0_1040
